# retention output loop: gain and first gate-row loads hoisted above the workgroup barrier that precedes the loop
# speedup vs baseline: 1.0003x; 1.0000x over previous
; #define LAS __attribute__((address_space(3)))
; __device__ __forceinline__ bf16_t f2bf(float f) { unsigned u = __builtin_bit_cast(unsigned, f); return (bf16_t)((u + 0x7fffu + ((u >> 16) & 1u)) >> 16); }
; __device__ __forceinline__ int crow(int r, int hi) { return (r & 3) + 8 * (r >> 2) + 4 * hi; }
; __device__ __forceinline__ int crow(int r, int hi) { return (r & 3) + 8 * (r >> 2) + 4 * hi; }
; template <int DK, int DV, bool MLSTM>
; __device__ __forceinline__ void out_unit2(LAS unsigned char* lds, LAS unsigned char* ldstab, const OutArgs a, const int wv) {
;     ...
; #pragma unroll
;     for (int r = 0; r < 16; ++r) {
;         const int row = 32 * rb + crow(r, hi);
;         const float t1 = s1[r] + exch[((1 - dh) * 128 + row) * 2], t2 = s2[r] + exch[((1 - dh) * 128 + row) * 2 + 1];
;         float mean, inv;
;         if (MLSTM) { mean = 0.f; inv = rsqrtf(t2 * (1.f / DV) + EPS); }
;         else { mean = t1 * (1.f / DV); inv = rsqrtf(fmaxf(t2 * (1.f / DV) - mean * mean, 0.f) + EPS); }
; #pragma unroll
;         for (int nb = 0; nb < NB; ++nb) { const int col = dh * (DV / 2) + 32 * nb + r32;
;             *(LAS bf16_t*)(lds + row * TP + col * 2) = f2bf((o[nb][r] - mean) * inv); }
;     }
.LBB0_1838:
	s_or_b64 exec, exec, s[4:5]
	v_lshlrev_b32_e32 v164, 1, v219
	v_subrev_u32_e32 v164, s6, v164
	s_add_i32 s4, 0, 0x22100
	v_lshl_add_u32 v164, v164, 2, s4
	s_waitcnt vmcnt(0) lgkmcnt(0)
	s_barrier
	ds_read_b128 v[164:167], v164 offset:1024
	v_lshlrev_b32_e32 v168, 1, v217
	v_subrev_u32_e32 v168, s6, v168
	v_lshl_add_u32 v168, v168, 2, s4
	ds_read2_b64 v[168:171], v168 offset0:128 offset1:129
	s_waitcnt lgkmcnt(1)
	v_pk_add_f32 v[156:157], v[156:157], v[164:165]
	s_nop 0
	v_pk_mul_f32 v[156:157], v[156:157], s[36:37] op_sel_hi:[1,0]
	s_nop 0
	v_fma_f32 v157, -v156, v156, v157
	v_max_f32_e32 v157, 0, v157
	v_add_f32_e32 v157, 0x358637bd, v157
	v_mul_f32_e32 v164, 0x4b800000, v157
	v_cmp_gt_f32_e32 vcc, s89, v157
	v_sub_f32_e32 v16, v16, v156
	v_sub_f32_e32 v0, v0, v156
	v_cndmask_b32_e32 v157, v157, v164, vcc
	v_rsq_f32_e32 v157, v157
	v_or_b32_e32 v164, s6, v233
	v_mul_f32_e32 v165, 0x45800000, v157
	v_cndmask_b32_e32 v157, v157, v165, vcc
	v_mul_f32_e32 v16, v16, v157
	v_bfe_u32 v172, v16, 16, 1
	v_lshlrev_b32_e32 v165, 10, v219
	v_add3_u32 v172, v16, v172, s90
	v_lshlrev_b32_e32 v16, 1, v164
	v_mul_f32_e32 v0, v0, v157
	v_add3_u32 v164, 0, v165, v16
	v_bfe_u32 v165, v0, 16, 1
	v_add3_u32 v0, v0, v165, s90
	ds_write_b16_d16_hi v164, v0 offset:64
	v_sub_f32_e32 v0, v32, v156
	v_mul_f32_e32 v0, v0, v157
	v_bfe_u32 v32, v0, 16, 1
	v_add3_u32 v0, v0, v32, s90
	ds_write_b16_d16_hi v164, v0 offset:128
	v_sub_f32_e32 v0, v48, v156
	v_mul_f32_e32 v0, v0, v157
	v_bfe_u32 v32, v0, 16, 1
	v_add3_u32 v0, v0, v32, s90
	ds_write_b16_d16_hi v164, v0 offset:192
	v_sub_f32_e32 v0, v96, v156
	v_mul_f32_e32 v0, v0, v157
	v_bfe_u32 v32, v0, 16, 1
	v_add3_u32 v0, v0, v32, s90
	ds_write_b16_d16_hi v164, v0 offset:256
	v_sub_f32_e32 v0, v112, v156
	v_mul_f32_e32 v0, v0, v157
	v_bfe_u32 v32, v0, 16, 1
	v_add3_u32 v0, v0, v32, s90
	ds_write_b16_d16_hi v164, v0 offset:320
	v_sub_f32_e32 v0, v80, v156
	v_mul_f32_e32 v0, v0, v157
	v_bfe_u32 v32, v0, 16, 1
	v_add3_u32 v0, v0, v32, s90
	ds_write_b16_d16_hi v164, v0 offset:384
	v_sub_f32_e32 v0, v64, v156
	v_mul_f32_e32 v0, v0, v157
	v_pk_add_f32 v[156:157], v[158:159], v[166:167]
	ds_write_b16_d16_hi v164, v172
	v_pk_mul_f32 v[156:157], v[156:157], s[36:37] op_sel_hi:[1,0]
	s_nop 0
	v_fma_f32 v32, -v156, v156, v157
	v_max_f32_e32 v32, 0, v32
	v_add_f32_e32 v32, 0x358637bd, v32
	v_mul_f32_e32 v48, 0x4b800000, v32
	v_cmp_gt_f32_e32 vcc, s89, v32
	v_sub_f32_e32 v17, v17, v156
	v_sub_f32_e32 v1, v1, v156
	v_cndmask_b32_e32 v32, v32, v48, vcc
	v_rsq_f32_e32 v32, v32
	v_bfe_u32 v48, v0, 16, 1
	v_add3_u32 v0, v0, v48, s90
	ds_write_b16_d16_hi v164, v0 offset:448
	v_mul_f32_e32 v0, 0x45800000, v32
	v_cndmask_b32_e32 v0, v32, v0, vcc
	v_mul_f32_e32 v17, v17, v0
	v_lshlrev_b32_e32 v32, 10, v218
	v_bfe_u32 v48, v17, 16, 1
	v_add3_u32 v17, v17, v48, s90
	v_add3_u32 v32, 0, v32, v16
	v_mul_f32_e32 v1, v1, v0
	ds_write_b16_d16_hi v32, v17
	v_bfe_u32 v17, v1, 16, 1
	v_add3_u32 v1, v1, v17, s90
	ds_write_b16_d16_hi v32, v1 offset:64
	v_sub_f32_e32 v1, v33, v156
	v_mul_f32_e32 v1, v1, v0
	v_bfe_u32 v17, v1, 16, 1
	v_add3_u32 v1, v1, v17, s90
	ds_write_b16_d16_hi v32, v1 offset:128
	v_sub_f32_e32 v1, v49, v156
	v_mul_f32_e32 v1, v1, v0
	v_bfe_u32 v17, v1, 16, 1
	v_add3_u32 v1, v1, v17, s90
	ds_write_b16_d16_hi v32, v1 offset:192
	v_sub_f32_e32 v1, v97, v156
	v_mul_f32_e32 v1, v1, v0
	v_bfe_u32 v17, v1, 16, 1
	v_add3_u32 v1, v1, v17, s90
	ds_write_b16_d16_hi v32, v1 offset:256
	v_sub_f32_e32 v1, v113, v156
	v_mul_f32_e32 v1, v1, v0
	v_bfe_u32 v17, v1, 16, 1
	v_add3_u32 v1, v1, v17, s90
	ds_write_b16_d16_hi v32, v1 offset:320
	v_sub_f32_e32 v1, v81, v156
	v_mul_f32_e32 v1, v1, v0
	v_bfe_u32 v17, v1, 16, 1
	v_add3_u32 v1, v1, v17, s90
	ds_write_b16_d16_hi v32, v1 offset:384
	v_sub_f32_e32 v1, v65, v156
	v_mul_f32_e32 v17, v1, v0
	s_waitcnt lgkmcnt(14)
	v_pk_add_f32 v[0:1], v[152:153], v[168:169]
	s_nop 0
	v_pk_mul_f32 v[0:1], v[0:1], s[36:37] op_sel_hi:[1,0]
	s_nop 0
	v_fma_f32 v1, -v0, v0, v1
	v_max_f32_e32 v1, 0, v1
	v_add_f32_e32 v1, 0x358637bd, v1
	v_mul_f32_e32 v33, 0x4b800000, v1
	v_cmp_gt_f32_e32 vcc, s89, v1
	v_sub_f32_e32 v18, v18, v0
	v_sub_f32_e32 v2, v2, v0
	v_cndmask_b32_e32 v1, v1, v33, vcc
	v_rsq_f32_e32 v1, v1
	v_bfe_u32 v33, v17, 16, 1
	v_add3_u32 v17, v17, v33, s90
	ds_write_b16_d16_hi v32, v17 offset:448
	v_mul_f32_e32 v17, 0x45800000, v1
	v_cndmask_b32_e32 v1, v1, v17, vcc
	v_mul_f32_e32 v18, v18, v1
	v_lshlrev_b32_e32 v17, 10, v217
	v_bfe_u32 v32, v18, 16, 1
	v_add3_u32 v18, v18, v32, s90
	v_add3_u32 v17, 0, v17, v16
	v_mul_f32_e32 v2, v2, v1
	ds_write_b16_d16_hi v17, v18
	v_bfe_u32 v18, v2, 16, 1
	v_add3_u32 v2, v2, v18, s90
	ds_write_b16_d16_hi v17, v2 offset:64
	v_sub_f32_e32 v2, v34, v0
	v_mul_f32_e32 v2, v2, v1
	v_bfe_u32 v18, v2, 16, 1
	v_add3_u32 v2, v2, v18, s90
	ds_write_b16_d16_hi v17, v2 offset:128
	v_sub_f32_e32 v2, v50, v0
	v_mul_f32_e32 v2, v2, v1
	v_bfe_u32 v18, v2, 16, 1
	v_add3_u32 v2, v2, v18, s90
	ds_write_b16_d16_hi v17, v2 offset:192
	v_sub_f32_e32 v2, v98, v0
	v_mul_f32_e32 v2, v2, v1
	v_bfe_u32 v18, v2, 16, 1
	v_add3_u32 v2, v2, v18, s90
	ds_write_b16_d16_hi v17, v2 offset:256
	v_sub_f32_e32 v2, v114, v0
	v_mul_f32_e32 v2, v2, v1
	v_bfe_u32 v18, v2, 16, 1
	v_add3_u32 v2, v2, v18, s90
	ds_write_b16_d16_hi v17, v2 offset:320
	v_sub_f32_e32 v2, v82, v0
	v_mul_f32_e32 v2, v2, v1
	v_bfe_u32 v18, v2, 16, 1
	v_add3_u32 v2, v2, v18, s90
	v_sub_f32_e32 v0, v66, v0
	ds_write_b16_d16_hi v17, v2 offset:384
	v_mul_f32_e32 v2, v0, v1
	v_pk_add_f32 v[0:1], v[154:155], v[170:171]
	s_nop 0
	v_pk_mul_f32 v[0:1], v[0:1], s[36:37] op_sel_hi:[1,0]
	s_nop 0
	v_fma_f32 v1, -v0, v0, v1
	v_max_f32_e32 v1, 0, v1
; #define LAS __attribute__((address_space(3)))
; __device__ __forceinline__ bf16_t f2bf(float f) { unsigned u = __builtin_bit_cast(unsigned, f); return (bf16_t)((u + 0x7fffu + ((u >> 16) & 1u)) >> 16); }
; __device__ __forceinline__ int crow(int r, int hi) { return (r & 3) + 8 * (r >> 2) + 4 * hi; }
; __device__ __forceinline__ int crow(int r, int hi) { return (r & 3) + 8 * (r >> 2) + 4 * hi; }
; template <int DK, int DV, bool MLSTM>
; __device__ __forceinline__ void out_unit2(LAS unsigned char* lds, LAS unsigned char* ldstab, const OutArgs a, const int wv) {
;     ...
; #pragma unroll
;     for (int r = 0; r < 16; ++r) {
;         const int row = 32 * rb + crow(r, hi);
;         const float t1 = s1[r] + exch[((1 - dh) * 128 + row) * 2], t2 = s2[r] + exch[((1 - dh) * 128 + row) * 2 + 1];
;         float mean, inv;
;         if (MLSTM) { mean = 0.f; inv = rsqrtf(t2 * (1.f / DV) + EPS); }
;         else { mean = t1 * (1.f / DV); inv = rsqrtf(fmaxf(t2 * (1.f / DV) - mean * mean, 0.f) + EPS); }
; #pragma unroll
;         for (int nb = 0; nb < NB; ++nb) { const int col = dh * (DV / 2) + 32 * nb + r32;
;             *(LAS bf16_t*)(lds + row * TP + col * 2) = f2bf((o[nb][r] - mean) * inv); }
;     }
	v_add_f32_e32 v1, 0x358637bd, v1
	v_mul_f32_e32 v18, 0x4b800000, v1
	v_cmp_gt_f32_e32 vcc, s89, v1
	s_nop 1
	v_cndmask_b32_e32 v1, v1, v18, vcc
	v_rsq_f32_e32 v1, v1
	v_bfe_u32 v18, v2, 16, 1
	v_add3_u32 v2, v2, v18, s90
	ds_write_b16_d16_hi v17, v2 offset:448
	v_mul_f32_e32 v2, 0x45800000, v1
	v_cndmask_b32_e32 v1, v1, v2, vcc
	v_sub_f32_e32 v17, v19, v0
	v_mul_f32_e32 v17, v17, v1
	v_lshlrev_b32_e32 v2, 10, v216
	v_bfe_u32 v18, v17, 16, 1
	v_add3_u32 v17, v17, v18, s90
	v_add3_u32 v18, 0, v2, v16
	v_sub_f32_e32 v2, v3, v0
	v_mul_f32_e32 v2, v2, v1
	v_bfe_u32 v3, v2, 16, 1
	v_add3_u32 v2, v2, v3, s90
	ds_write_b16_d16_hi v18, v2 offset:64
	v_sub_f32_e32 v2, v35, v0
	v_mul_f32_e32 v2, v2, v1
	v_bfe_u32 v3, v2, 16, 1
	v_add3_u32 v2, v2, v3, s90
	ds_write_b16_d16_hi v18, v2 offset:128
	v_sub_f32_e32 v2, v51, v0
	v_mul_f32_e32 v2, v2, v1
	v_bfe_u32 v3, v2, 16, 1
	v_add3_u32 v2, v2, v3, s90
	ds_write_b16_d16_hi v18, v2 offset:192
	v_sub_f32_e32 v2, v99, v0
	v_mul_f32_e32 v2, v2, v1
	v_bfe_u32 v3, v2, 16, 1
	v_add3_u32 v2, v2, v3, s90
	ds_write_b16_d16_hi v18, v2 offset:256
	v_sub_f32_e32 v2, v115, v0
	v_mul_f32_e32 v2, v2, v1
	v_bfe_u32 v3, v2, 16, 1
	v_add3_u32 v2, v2, v3, s90
	ds_write_b16_d16_hi v18, v2 offset:320
	v_sub_f32_e32 v2, v83, v0
	v_sub_f32_e32 v0, v67, v0
	ds_write_b16_d16_hi v18, v17
	v_mul_f32_e32 v2, v2, v1
	v_mul_f32_e32 v17, v0, v1
	v_lshlrev_b32_e32 v0, 1, v215
	v_bfe_u32 v3, v2, 16, 1
	v_subrev_u32_e32 v0, s6, v0
	v_add3_u32 v2, v2, v3, s90
	v_lshl_add_u32 v0, v0, 2, s4
	ds_write_b16_d16_hi v18, v2 offset:384
	ds_read2_b64 v[0:3], v0 offset0:128 offset1:129
	v_lshlrev_b32_e32 v19, 1, v213
	v_subrev_u32_e32 v19, s6, v19
	v_lshl_add_u32 v19, v19, 2, s4
	ds_read2_b64 v[32:35], v19 offset0:128 offset1:129
	s_waitcnt lgkmcnt(1)
	v_pk_add_f32 v[0:1], v[148:149], v[0:1]
	s_nop 0
	v_pk_mul_f32 v[0:1], v[0:1], s[36:37] op_sel_hi:[1,0]
	s_nop 0
	v_fma_f32 v1, -v0, v0, v1
	v_max_f32_e32 v1, 0, v1
	v_add_f32_e32 v1, 0x358637bd, v1
	v_mul_f32_e32 v19, 0x4b800000, v1
	v_cmp_gt_f32_e32 vcc, s89, v1
	v_sub_f32_e32 v4, v4, v0
	s_nop 0
	v_cndmask_b32_e32 v1, v1, v19, vcc
	v_rsq_f32_e32 v1, v1
	v_bfe_u32 v19, v17, 16, 1
	v_add3_u32 v17, v17, v19, s90
	ds_write_b16_d16_hi v18, v17 offset:448
	v_mul_f32_e32 v17, 0x45800000, v1
	v_cndmask_b32_e32 v1, v1, v17, vcc
	v_sub_f32_e32 v18, v20, v0
	v_mul_f32_e32 v18, v18, v1
	v_lshlrev_b32_e32 v17, 10, v215
	v_bfe_u32 v19, v18, 16, 1
	v_add3_u32 v18, v18, v19, s90
	v_add3_u32 v17, 0, v17, v16
	v_mul_f32_e32 v4, v4, v1
	ds_write_b16_d16_hi v17, v18
	v_bfe_u32 v18, v4, 16, 1
	v_add3_u32 v4, v4, v18, s90
	ds_write_b16_d16_hi v17, v4 offset:64
	v_sub_f32_e32 v4, v36, v0
	v_mul_f32_e32 v4, v4, v1
	v_bfe_u32 v18, v4, 16, 1
	v_add3_u32 v4, v4, v18, s90
	ds_write_b16_d16_hi v17, v4 offset:128
	v_sub_f32_e32 v4, v52, v0
	v_mul_f32_e32 v4, v4, v1
	v_bfe_u32 v18, v4, 16, 1
	v_add3_u32 v4, v4, v18, s90
	ds_write_b16_d16_hi v17, v4 offset:192
	v_sub_f32_e32 v4, v100, v0
	v_mul_f32_e32 v4, v4, v1
	v_bfe_u32 v18, v4, 16, 1
	v_add3_u32 v4, v4, v18, s90
	ds_write_b16_d16_hi v17, v4 offset:256
	v_sub_f32_e32 v4, v116, v0
	v_mul_f32_e32 v4, v4, v1
	v_bfe_u32 v18, v4, 16, 1
	v_add3_u32 v4, v4, v18, s90
	ds_write_b16_d16_hi v17, v4 offset:320
	v_sub_f32_e32 v4, v84, v0
	v_mul_f32_e32 v4, v4, v1
	v_bfe_u32 v18, v4, 16, 1
	v_add3_u32 v4, v4, v18, s90
	v_sub_f32_e32 v0, v68, v0
	ds_write_b16_d16_hi v17, v4 offset:384
	v_mul_f32_e32 v4, v0, v1
	v_pk_add_f32 v[0:1], v[150:151], v[2:3]
	s_nop 0
	v_pk_mul_f32 v[0:1], v[0:1], s[36:37] op_sel_hi:[1,0]
	s_nop 0
	v_fma_f32 v1, -v0, v0, v1
	v_max_f32_e32 v1, 0, v1
	v_add_f32_e32 v1, 0x358637bd, v1
	v_mul_f32_e32 v2, 0x4b800000, v1
	v_cmp_gt_f32_e32 vcc, s89, v1
	v_sub_f32_e32 v3, v21, v0
	s_nop 0
	v_cndmask_b32_e32 v1, v1, v2, vcc
	v_rsq_f32_e32 v1, v1
	v_bfe_u32 v2, v4, 16, 1
	v_add3_u32 v2, v4, v2, s90
	ds_write_b16_d16_hi v17, v2 offset:448
	v_mul_f32_e32 v2, 0x45800000, v1
	v_cndmask_b32_e32 v1, v1, v2, vcc
	v_mul_f32_e32 v3, v3, v1
	v_lshlrev_b32_e32 v2, 10, v214
	v_bfe_u32 v4, v3, 16, 1
	v_add3_u32 v3, v3, v4, s90
	v_add3_u32 v2, 0, v2, v16
	ds_write_b16_d16_hi v2, v3
	v_sub_f32_e32 v3, v5, v0
	v_mul_f32_e32 v3, v3, v1
	v_bfe_u32 v4, v3, 16, 1
	v_add3_u32 v3, v3, v4, s90
	ds_write_b16_d16_hi v2, v3 offset:64
	v_sub_f32_e32 v3, v37, v0
	v_mul_f32_e32 v3, v3, v1
	v_bfe_u32 v4, v3, 16, 1
	v_add3_u32 v3, v3, v4, s90
	ds_write_b16_d16_hi v2, v3 offset:128
	v_sub_f32_e32 v3, v53, v0
	v_mul_f32_e32 v3, v3, v1
	v_bfe_u32 v4, v3, 16, 1
	v_add3_u32 v3, v3, v4, s90
	ds_write_b16_d16_hi v2, v3 offset:192
	v_sub_f32_e32 v3, v101, v0
	v_mul_f32_e32 v3, v3, v1
	v_bfe_u32 v4, v3, 16, 1
	v_add3_u32 v3, v3, v4, s90
	ds_write_b16_d16_hi v2, v3 offset:256
	v_sub_f32_e32 v3, v117, v0
	v_mul_f32_e32 v3, v3, v1
	v_bfe_u32 v4, v3, 16, 1
	v_add3_u32 v3, v3, v4, s90
	ds_write_b16_d16_hi v2, v3 offset:320
	v_sub_f32_e32 v3, v85, v0
	v_mul_f32_e32 v3, v3, v1
	v_bfe_u32 v4, v3, 16, 1
	v_add3_u32 v3, v3, v4, s90
	v_sub_f32_e32 v0, v69, v0
	ds_write_b16_d16_hi v2, v3 offset:384
	v_mul_f32_e32 v3, v0, v1
	s_waitcnt lgkmcnt(14)
; #define LAS __attribute__((address_space(3)))
; __device__ __forceinline__ bf16_t f2bf(float f) { unsigned u = __builtin_bit_cast(unsigned, f); return (bf16_t)((u + 0x7fffu + ((u >> 16) & 1u)) >> 16); }
; __device__ __forceinline__ int crow(int r, int hi) { return (r & 3) + 8 * (r >> 2) + 4 * hi; }
; __device__ __forceinline__ int crow(int r, int hi) { return (r & 3) + 8 * (r >> 2) + 4 * hi; }
; template <int DK, int DV, bool MLSTM>
; __device__ __forceinline__ void out_unit2(LAS unsigned char* lds, LAS unsigned char* ldstab, const OutArgs a, const int wv) {
;     ...
; #pragma unroll
;     for (int r = 0; r < 16; ++r) {
;         const int row = 32 * rb + crow(r, hi);
;         const float t1 = s1[r] + exch[((1 - dh) * 128 + row) * 2], t2 = s2[r] + exch[((1 - dh) * 128 + row) * 2 + 1];
;         float mean, inv;
;         if (MLSTM) { mean = 0.f; inv = rsqrtf(t2 * (1.f / DV) + EPS); }
;         else { mean = t1 * (1.f / DV); inv = rsqrtf(fmaxf(t2 * (1.f / DV) - mean * mean, 0.f) + EPS); }
; #pragma unroll
;         for (int nb = 0; nb < NB; ++nb) { const int col = dh * (DV / 2) + 32 * nb + r32;
;             *(LAS bf16_t*)(lds + row * TP + col * 2) = f2bf((o[nb][r] - mean) * inv); }
;     }
	v_pk_add_f32 v[0:1], v[144:145], v[32:33]
	s_nop 0
	v_pk_mul_f32 v[0:1], v[0:1], s[36:37] op_sel_hi:[1,0]
	s_nop 0
	v_fma_f32 v1, -v0, v0, v1
	v_max_f32_e32 v1, 0, v1
	v_add_f32_e32 v1, 0x358637bd, v1
	v_mul_f32_e32 v4, 0x4b800000, v1
	v_cmp_gt_f32_e32 vcc, s89, v1
	s_nop 1
	v_cndmask_b32_e32 v1, v1, v4, vcc
	v_rsq_f32_e32 v1, v1
	v_bfe_u32 v4, v3, 16, 1
	v_add3_u32 v3, v3, v4, s90
	ds_write_b16_d16_hi v2, v3 offset:448
	v_mul_f32_e32 v2, 0x45800000, v1
	v_cndmask_b32_e32 v1, v1, v2, vcc
	v_sub_f32_e32 v3, v22, v0
	v_mul_f32_e32 v3, v3, v1
	v_lshlrev_b32_e32 v2, 10, v213
	v_bfe_u32 v4, v3, 16, 1
	v_add3_u32 v3, v3, v4, s90
	v_add3_u32 v2, 0, v2, v16
	ds_write_b16_d16_hi v2, v3
	v_sub_f32_e32 v3, v6, v0
	v_mul_f32_e32 v3, v3, v1
	v_bfe_u32 v4, v3, 16, 1
	v_add3_u32 v3, v3, v4, s90
	ds_write_b16_d16_hi v2, v3 offset:64
	v_sub_f32_e32 v3, v38, v0
	v_mul_f32_e32 v3, v3, v1
	v_bfe_u32 v4, v3, 16, 1
	v_add3_u32 v3, v3, v4, s90
	ds_write_b16_d16_hi v2, v3 offset:128
	v_sub_f32_e32 v3, v54, v0
	v_mul_f32_e32 v3, v3, v1
	v_bfe_u32 v4, v3, 16, 1
	v_add3_u32 v3, v3, v4, s90
	ds_write_b16_d16_hi v2, v3 offset:192
	v_sub_f32_e32 v3, v102, v0
	v_mul_f32_e32 v3, v3, v1
	v_bfe_u32 v4, v3, 16, 1
	v_add3_u32 v3, v3, v4, s90
	ds_write_b16_d16_hi v2, v3 offset:256
	v_sub_f32_e32 v3, v118, v0
	v_mul_f32_e32 v3, v3, v1
	v_bfe_u32 v4, v3, 16, 1
	v_add3_u32 v3, v3, v4, s90
	ds_write_b16_d16_hi v2, v3 offset:320
	v_sub_f32_e32 v3, v86, v0
	v_mul_f32_e32 v3, v3, v1
	v_bfe_u32 v4, v3, 16, 1
	v_add3_u32 v3, v3, v4, s90
	v_sub_f32_e32 v0, v70, v0
	ds_write_b16_d16_hi v2, v3 offset:384
	v_mul_f32_e32 v3, v0, v1
	v_pk_add_f32 v[0:1], v[146:147], v[34:35]
	s_nop 0
	v_pk_mul_f32 v[0:1], v[0:1], s[36:37] op_sel_hi:[1,0]
	s_nop 0
	v_fma_f32 v1, -v0, v0, v1
	v_max_f32_e32 v1, 0, v1
	v_add_f32_e32 v1, 0x358637bd, v1
	v_mul_f32_e32 v4, 0x4b800000, v1
	v_cmp_gt_f32_e32 vcc, s89, v1
	s_nop 1
	v_cndmask_b32_e32 v1, v1, v4, vcc
	v_rsq_f32_e32 v1, v1
	v_bfe_u32 v4, v3, 16, 1
	v_add3_u32 v3, v3, v4, s90
	ds_write_b16_d16_hi v2, v3 offset:448
	v_mul_f32_e32 v2, 0x45800000, v1
	v_cndmask_b32_e32 v1, v1, v2, vcc
	v_sub_f32_e32 v3, v23, v0
	v_lshlrev_b32_e32 v2, 10, v212
	v_mul_f32_e32 v3, v3, v1
	v_bfe_u32 v4, v3, 16, 1
	v_add3_u32 v17, 0, v2, v16
	v_sub_f32_e32 v2, v7, v0
	v_add3_u32 v3, v3, v4, s90
	v_mul_f32_e32 v2, v2, v1
	ds_write_b16_d16_hi v17, v3
	v_bfe_u32 v3, v2, 16, 1
	v_add3_u32 v2, v2, v3, s90
	ds_write_b16_d16_hi v17, v2 offset:64
	v_sub_f32_e32 v2, v39, v0
	v_mul_f32_e32 v2, v2, v1
	v_bfe_u32 v3, v2, 16, 1
	v_add3_u32 v2, v2, v3, s90
	ds_write_b16_d16_hi v17, v2 offset:128
	v_sub_f32_e32 v2, v55, v0
	v_mul_f32_e32 v2, v2, v1
	v_bfe_u32 v3, v2, 16, 1
	v_add3_u32 v2, v2, v3, s90
	ds_write_b16_d16_hi v17, v2 offset:192
	v_sub_f32_e32 v2, v103, v0
	v_mul_f32_e32 v2, v2, v1
	v_bfe_u32 v3, v2, 16, 1
	v_add3_u32 v2, v2, v3, s90
	ds_write_b16_d16_hi v17, v2 offset:256
	v_sub_f32_e32 v2, v119, v0
	v_mul_f32_e32 v2, v2, v1
	v_bfe_u32 v3, v2, 16, 1
	v_add3_u32 v2, v2, v3, s90
	ds_write_b16_d16_hi v17, v2 offset:320
	v_sub_f32_e32 v2, v87, v0
	v_sub_f32_e32 v0, v71, v0
	v_mul_f32_e32 v2, v2, v1
	v_mul_f32_e32 v18, v0, v1
	v_lshlrev_b32_e32 v0, 1, v211
	v_bfe_u32 v3, v2, 16, 1
	v_subrev_u32_e32 v0, s6, v0
	v_add3_u32 v2, v2, v3, s90
	v_lshl_add_u32 v0, v0, 2, s4
	ds_write_b16_d16_hi v17, v2 offset:384
	ds_read2_b64 v[0:3], v0 offset0:128 offset1:129
	v_lshlrev_b32_e32 v4, 1, v209
	v_subrev_u32_e32 v4, s6, v4
	v_lshl_add_u32 v4, v4, 2, s4
	ds_read2_b64 v[4:7], v4 offset0:128 offset1:129
	s_waitcnt lgkmcnt(1)
	v_pk_add_f32 v[0:1], v[140:141], v[0:1]
	s_nop 0
	v_pk_mul_f32 v[0:1], v[0:1], s[36:37] op_sel_hi:[1,0]
	s_nop 0
	v_fma_f32 v1, -v0, v0, v1
	v_max_f32_e32 v1, 0, v1
	v_add_f32_e32 v1, 0x358637bd, v1
	v_mul_f32_e32 v19, 0x4b800000, v1
	v_cmp_gt_f32_e32 vcc, s89, v1
	v_sub_f32_e32 v8, v8, v0
	s_nop 0
	v_cndmask_b32_e32 v1, v1, v19, vcc
	v_rsq_f32_e32 v1, v1
	v_bfe_u32 v19, v18, 16, 1
	v_add3_u32 v18, v18, v19, s90
	ds_write_b16_d16_hi v17, v18 offset:448
	v_mul_f32_e32 v17, 0x45800000, v1
	v_cndmask_b32_e32 v1, v1, v17, vcc
	v_sub_f32_e32 v18, v24, v0
	v_mul_f32_e32 v18, v18, v1
	v_lshlrev_b32_e32 v17, 10, v211
	v_bfe_u32 v19, v18, 16, 1
	v_add3_u32 v18, v18, v19, s90
	v_add3_u32 v17, 0, v17, v16
	v_mul_f32_e32 v8, v8, v1
	ds_write_b16_d16_hi v17, v18
	v_bfe_u32 v18, v8, 16, 1
	v_add3_u32 v8, v8, v18, s90
	ds_write_b16_d16_hi v17, v8 offset:64
	v_sub_f32_e32 v8, v40, v0
	v_mul_f32_e32 v8, v8, v1
	v_bfe_u32 v18, v8, 16, 1
	v_add3_u32 v8, v8, v18, s90
	ds_write_b16_d16_hi v17, v8 offset:128
	v_sub_f32_e32 v8, v56, v0
	v_mul_f32_e32 v8, v8, v1
	v_bfe_u32 v18, v8, 16, 1
	v_add3_u32 v8, v8, v18, s90
	ds_write_b16_d16_hi v17, v8 offset:192
	v_sub_f32_e32 v8, v104, v0
	v_mul_f32_e32 v8, v8, v1
	v_bfe_u32 v18, v8, 16, 1
	v_add3_u32 v8, v8, v18, s90
	ds_write_b16_d16_hi v17, v8 offset:256
	v_sub_f32_e32 v8, v120, v0
	v_mul_f32_e32 v8, v8, v1
	v_bfe_u32 v18, v8, 16, 1
	v_add3_u32 v8, v8, v18, s90
	ds_write_b16_d16_hi v17, v8 offset:320
	v_sub_f32_e32 v8, v88, v0
	v_mul_f32_e32 v8, v8, v1
	v_bfe_u32 v18, v8, 16, 1
	v_add3_u32 v8, v8, v18, s90
	v_sub_f32_e32 v0, v72, v0
	ds_write_b16_d16_hi v17, v8 offset:384
	v_mul_f32_e32 v8, v0, v1
	v_pk_add_f32 v[0:1], v[142:143], v[2:3]
	s_nop 0
	v_pk_mul_f32 v[0:1], v[0:1], s[36:37] op_sel_hi:[1,0]
	s_nop 0
	v_fma_f32 v1, -v0, v0, v1
	v_max_f32_e32 v1, 0, v1
	v_add_f32_e32 v1, 0x358637bd, v1
	v_mul_f32_e32 v2, 0x4b800000, v1
	v_cmp_gt_f32_e32 vcc, s89, v1
	v_sub_f32_e32 v3, v25, v0
	s_nop 0
	v_cndmask_b32_e32 v1, v1, v2, vcc
	v_rsq_f32_e32 v1, v1
	v_bfe_u32 v2, v8, 16, 1
	v_add3_u32 v2, v8, v2, s90
	ds_write_b16_d16_hi v17, v2 offset:448
	v_mul_f32_e32 v2, 0x45800000, v1
	v_cndmask_b32_e32 v1, v1, v2, vcc
	v_mul_f32_e32 v3, v3, v1
	v_lshlrev_b32_e32 v2, 10, v210
	v_bfe_u32 v8, v3, 16, 1
	v_add3_u32 v3, v3, v8, s90
	v_add3_u32 v2, 0, v2, v16
	ds_write_b16_d16_hi v2, v3
	v_sub_f32_e32 v3, v9, v0
	v_mul_f32_e32 v3, v3, v1
	v_bfe_u32 v8, v3, 16, 1
	v_add3_u32 v3, v3, v8, s90
	ds_write_b16_d16_hi v2, v3 offset:64
	v_sub_f32_e32 v3, v41, v0
	v_mul_f32_e32 v3, v3, v1
	v_bfe_u32 v8, v3, 16, 1
	v_add3_u32 v3, v3, v8, s90
	ds_write_b16_d16_hi v2, v3 offset:128
	v_sub_f32_e32 v3, v57, v0
	v_mul_f32_e32 v3, v3, v1
	v_bfe_u32 v8, v3, 16, 1
	v_add3_u32 v3, v3, v8, s90
	ds_write_b16_d16_hi v2, v3 offset:192
	v_sub_f32_e32 v3, v105, v0
	v_mul_f32_e32 v3, v3, v1
	v_bfe_u32 v8, v3, 16, 1
	v_add3_u32 v3, v3, v8, s90
	ds_write_b16_d16_hi v2, v3 offset:256
	v_sub_f32_e32 v3, v121, v0
	v_mul_f32_e32 v3, v3, v1
	v_bfe_u32 v8, v3, 16, 1
	v_add3_u32 v3, v3, v8, s90
	ds_write_b16_d16_hi v2, v3 offset:320
	v_sub_f32_e32 v3, v89, v0
	v_mul_f32_e32 v3, v3, v1
	v_bfe_u32 v8, v3, 16, 1
	v_add3_u32 v3, v3, v8, s90
	v_sub_f32_e32 v0, v73, v0
	ds_write_b16_d16_hi v2, v3 offset:384
	v_mul_f32_e32 v3, v0, v1
	s_waitcnt lgkmcnt(14)
; #define LAS __attribute__((address_space(3)))
; __device__ __forceinline__ bf16_t f2bf(float f) { unsigned u = __builtin_bit_cast(unsigned, f); return (bf16_t)((u + 0x7fffu + ((u >> 16) & 1u)) >> 16); }
; __device__ __forceinline__ int crow(int r, int hi) { return (r & 3) + 8 * (r >> 2) + 4 * hi; }
; __device__ __forceinline__ int crow(int r, int hi) { return (r & 3) + 8 * (r >> 2) + 4 * hi; }
; template <int DK, int DV, bool MLSTM>
; __device__ __forceinline__ void out_unit2(LAS unsigned char* lds, LAS unsigned char* ldstab, const OutArgs a, const int wv) {
;     ...
; #pragma unroll
;     for (int r = 0; r < 16; ++r) {
;         const int row = 32 * rb + crow(r, hi);
;         const float t1 = s1[r] + exch[((1 - dh) * 128 + row) * 2], t2 = s2[r] + exch[((1 - dh) * 128 + row) * 2 + 1];
;         float mean, inv;
;         if (MLSTM) { mean = 0.f; inv = rsqrtf(t2 * (1.f / DV) + EPS); }
;         else { mean = t1 * (1.f / DV); inv = rsqrtf(fmaxf(t2 * (1.f / DV) - mean * mean, 0.f) + EPS); }
; #pragma unroll
;         for (int nb = 0; nb < NB; ++nb) { const int col = dh * (DV / 2) + 32 * nb + r32;
;             *(LAS bf16_t*)(lds + row * TP + col * 2) = f2bf((o[nb][r] - mean) * inv); }
;     }
	v_pk_add_f32 v[0:1], v[136:137], v[4:5]
	s_nop 0
	v_pk_mul_f32 v[0:1], v[0:1], s[36:37] op_sel_hi:[1,0]
	s_nop 0
	v_fma_f32 v1, -v0, v0, v1
	v_max_f32_e32 v1, 0, v1
	v_add_f32_e32 v1, 0x358637bd, v1
	v_mul_f32_e32 v4, 0x4b800000, v1
	v_cmp_gt_f32_e32 vcc, s89, v1
	s_nop 1
	v_cndmask_b32_e32 v1, v1, v4, vcc
	v_rsq_f32_e32 v1, v1
	v_bfe_u32 v4, v3, 16, 1
	v_add3_u32 v3, v3, v4, s90
	ds_write_b16_d16_hi v2, v3 offset:448
	v_mul_f32_e32 v2, 0x45800000, v1
	v_cndmask_b32_e32 v1, v1, v2, vcc
	v_sub_f32_e32 v3, v26, v0
	v_mul_f32_e32 v3, v3, v1
	v_lshlrev_b32_e32 v2, 10, v209
	v_bfe_u32 v4, v3, 16, 1
	v_add3_u32 v3, v3, v4, s90
	v_add3_u32 v2, 0, v2, v16
	ds_write_b16_d16_hi v2, v3
	v_sub_f32_e32 v3, v10, v0
	v_mul_f32_e32 v3, v3, v1
	v_bfe_u32 v4, v3, 16, 1
	v_add3_u32 v3, v3, v4, s90
	ds_write_b16_d16_hi v2, v3 offset:64
	v_sub_f32_e32 v3, v42, v0
	v_mul_f32_e32 v3, v3, v1
	v_bfe_u32 v4, v3, 16, 1
	v_add3_u32 v3, v3, v4, s90
	ds_write_b16_d16_hi v2, v3 offset:128
	v_sub_f32_e32 v3, v58, v0
	v_mul_f32_e32 v3, v3, v1
	v_bfe_u32 v4, v3, 16, 1
	v_add3_u32 v3, v3, v4, s90
	ds_write_b16_d16_hi v2, v3 offset:192
	v_sub_f32_e32 v3, v106, v0
	v_mul_f32_e32 v3, v3, v1
	v_bfe_u32 v4, v3, 16, 1
	v_add3_u32 v3, v3, v4, s90
	ds_write_b16_d16_hi v2, v3 offset:256
	v_sub_f32_e32 v3, v122, v0
	v_mul_f32_e32 v3, v3, v1
	v_bfe_u32 v4, v3, 16, 1
	v_add3_u32 v3, v3, v4, s90
	ds_write_b16_d16_hi v2, v3 offset:320
	v_sub_f32_e32 v3, v90, v0
	v_mul_f32_e32 v3, v3, v1
	v_bfe_u32 v4, v3, 16, 1
	v_add3_u32 v3, v3, v4, s90
	v_sub_f32_e32 v0, v74, v0
	ds_write_b16_d16_hi v2, v3 offset:384
	v_mul_f32_e32 v3, v0, v1
	v_pk_add_f32 v[0:1], v[138:139], v[6:7]
	s_nop 0
	v_pk_mul_f32 v[0:1], v[0:1], s[36:37] op_sel_hi:[1,0]
	s_nop 0
	v_fma_f32 v1, -v0, v0, v1
	v_max_f32_e32 v1, 0, v1
	v_add_f32_e32 v1, 0x358637bd, v1
	v_mul_f32_e32 v4, 0x4b800000, v1
	v_cmp_gt_f32_e32 vcc, s89, v1
	s_nop 1
	v_cndmask_b32_e32 v1, v1, v4, vcc
	v_rsq_f32_e32 v1, v1
	v_bfe_u32 v4, v3, 16, 1
	v_add3_u32 v3, v3, v4, s90
	ds_write_b16_d16_hi v2, v3 offset:448
	v_mul_f32_e32 v2, 0x45800000, v1
	v_cndmask_b32_e32 v1, v1, v2, vcc
	v_sub_f32_e32 v3, v27, v0
	v_lshlrev_b32_e32 v2, 10, v208
	v_mul_f32_e32 v3, v3, v1
	v_bfe_u32 v4, v3, 16, 1
	v_add3_u32 v8, 0, v2, v16
	v_sub_f32_e32 v2, v11, v0
	v_add3_u32 v3, v3, v4, s90
	v_mul_f32_e32 v2, v2, v1
	ds_write_b16_d16_hi v8, v3
	v_bfe_u32 v3, v2, 16, 1
	v_add3_u32 v2, v2, v3, s90
	ds_write_b16_d16_hi v8, v2 offset:64
	v_sub_f32_e32 v2, v43, v0
	v_mul_f32_e32 v2, v2, v1
	v_bfe_u32 v3, v2, 16, 1
	v_add3_u32 v2, v2, v3, s90
	ds_write_b16_d16_hi v8, v2 offset:128
	v_sub_f32_e32 v2, v59, v0
	v_mul_f32_e32 v2, v2, v1
	v_bfe_u32 v3, v2, 16, 1
	v_add3_u32 v2, v2, v3, s90
	ds_write_b16_d16_hi v8, v2 offset:192
	v_sub_f32_e32 v2, v107, v0
	v_mul_f32_e32 v2, v2, v1
	v_bfe_u32 v3, v2, 16, 1
	v_add3_u32 v2, v2, v3, s90
	ds_write_b16_d16_hi v8, v2 offset:256
	v_sub_f32_e32 v2, v123, v0
	v_mul_f32_e32 v2, v2, v1
	v_bfe_u32 v3, v2, 16, 1
	v_add3_u32 v2, v2, v3, s90
	ds_write_b16_d16_hi v8, v2 offset:320
	v_sub_f32_e32 v2, v91, v0
	v_sub_f32_e32 v0, v75, v0
	v_mul_f32_e32 v2, v2, v1
	v_mul_f32_e32 v9, v0, v1
	v_lshlrev_b32_e32 v0, 1, v207
	v_bfe_u32 v3, v2, 16, 1
	v_subrev_u32_e32 v0, s6, v0
	v_add3_u32 v2, v2, v3, s90
	v_lshl_add_u32 v0, v0, 2, s4
	ds_write_b16_d16_hi v8, v2 offset:384
	ds_read2_b64 v[0:3], v0 offset0:128 offset1:129
	v_lshlrev_b32_e32 v4, 1, v162
	v_subrev_u32_e32 v4, s6, v4
	v_lshl_add_u32 v4, v4, 2, s4
	ds_read2_b64 v[4:7], v4 offset0:128 offset1:129
	s_waitcnt lgkmcnt(1)
	v_pk_add_f32 v[0:1], v[132:133], v[0:1]
	s_nop 0
	v_pk_mul_f32 v[0:1], v[0:1], s[36:37] op_sel_hi:[1,0]
	s_nop 0
	v_fma_f32 v1, -v0, v0, v1
	v_max_f32_e32 v1, 0, v1
	v_add_f32_e32 v1, 0x358637bd, v1
	v_mul_f32_e32 v10, 0x4b800000, v1
	v_cmp_gt_f32_e32 vcc, s89, v1
	s_nop 1
	v_cndmask_b32_e32 v1, v1, v10, vcc
	v_rsq_f32_e32 v1, v1
	v_bfe_u32 v10, v9, 16, 1
	v_add3_u32 v9, v9, v10, s90
	ds_write_b16_d16_hi v8, v9 offset:448
	v_mul_f32_e32 v8, 0x45800000, v1
	v_cndmask_b32_e32 v1, v1, v8, vcc
	v_sub_f32_e32 v9, v28, v0
	v_mul_f32_e32 v9, v9, v1
	v_lshlrev_b32_e32 v8, 10, v207
	v_bfe_u32 v10, v9, 16, 1
	v_add3_u32 v9, v9, v10, s90
	v_add3_u32 v8, 0, v8, v16
	ds_write_b16_d16_hi v8, v9
	v_sub_f32_e32 v9, v12, v0
	v_mul_f32_e32 v9, v9, v1
	v_bfe_u32 v10, v9, 16, 1
	v_add3_u32 v9, v9, v10, s90
	ds_write_b16_d16_hi v8, v9 offset:64
	v_sub_f32_e32 v9, v44, v0
	v_mul_f32_e32 v9, v9, v1
	v_bfe_u32 v10, v9, 16, 1
	v_add3_u32 v9, v9, v10, s90
	ds_write_b16_d16_hi v8, v9 offset:128
	v_sub_f32_e32 v9, v60, v0
	v_mul_f32_e32 v9, v9, v1
	v_bfe_u32 v10, v9, 16, 1
	v_add3_u32 v9, v9, v10, s90
	ds_write_b16_d16_hi v8, v9 offset:192
	v_sub_f32_e32 v9, v108, v0
	v_mul_f32_e32 v9, v9, v1
	v_bfe_u32 v10, v9, 16, 1
	v_add3_u32 v9, v9, v10, s90
	ds_write_b16_d16_hi v8, v9 offset:256
	v_sub_f32_e32 v9, v124, v0
	v_mul_f32_e32 v9, v9, v1
	v_bfe_u32 v10, v9, 16, 1
	v_add3_u32 v9, v9, v10, s90
	ds_write_b16_d16_hi v8, v9 offset:320
	v_sub_f32_e32 v9, v92, v0
	v_mul_f32_e32 v9, v9, v1
	v_bfe_u32 v10, v9, 16, 1
	v_add3_u32 v9, v9, v10, s90
	v_sub_f32_e32 v0, v76, v0
	ds_write_b16_d16_hi v8, v9 offset:384
	v_mul_f32_e32 v9, v0, v1
	v_pk_add_f32 v[0:1], v[134:135], v[2:3]
	s_nop 0
	v_pk_mul_f32 v[0:1], v[0:1], s[36:37] op_sel_hi:[1,0]
	s_nop 0
	v_fma_f32 v1, -v0, v0, v1
	v_max_f32_e32 v1, 0, v1
	v_add_f32_e32 v1, 0x358637bd, v1
	v_mul_f32_e32 v2, 0x4b800000, v1
	v_cmp_gt_f32_e32 vcc, s89, v1
	v_sub_f32_e32 v3, v29, v0
	s_nop 0
	v_cndmask_b32_e32 v1, v1, v2, vcc
	v_rsq_f32_e32 v1, v1
	v_bfe_u32 v2, v9, 16, 1
	v_add3_u32 v2, v9, v2, s90
	ds_write_b16_d16_hi v8, v2 offset:448
	v_mul_f32_e32 v2, 0x45800000, v1
	v_cndmask_b32_e32 v1, v1, v2, vcc
	v_mul_f32_e32 v3, v3, v1
	v_lshlrev_b32_e32 v2, 10, v206
	v_bfe_u32 v8, v3, 16, 1
	v_add3_u32 v3, v3, v8, s90
	v_add3_u32 v2, 0, v2, v16
	ds_write_b16_d16_hi v2, v3
	v_sub_f32_e32 v3, v13, v0
	v_mul_f32_e32 v3, v3, v1
	v_bfe_u32 v8, v3, 16, 1
	v_add3_u32 v3, v3, v8, s90
	ds_write_b16_d16_hi v2, v3 offset:64
	v_sub_f32_e32 v3, v45, v0
	v_mul_f32_e32 v3, v3, v1
	v_bfe_u32 v8, v3, 16, 1
	v_add3_u32 v3, v3, v8, s90
	ds_write_b16_d16_hi v2, v3 offset:128
	v_sub_f32_e32 v3, v61, v0
	v_mul_f32_e32 v3, v3, v1
	v_bfe_u32 v8, v3, 16, 1
	v_add3_u32 v3, v3, v8, s90
	ds_write_b16_d16_hi v2, v3 offset:192
	v_sub_f32_e32 v3, v109, v0
	v_mul_f32_e32 v3, v3, v1
	v_bfe_u32 v8, v3, 16, 1
	v_add3_u32 v3, v3, v8, s90
	ds_write_b16_d16_hi v2, v3 offset:256
	v_sub_f32_e32 v3, v125, v0
	v_mul_f32_e32 v3, v3, v1
	v_bfe_u32 v8, v3, 16, 1
	v_add3_u32 v3, v3, v8, s90
	ds_write_b16_d16_hi v2, v3 offset:320
	v_sub_f32_e32 v3, v93, v0
	v_mul_f32_e32 v3, v3, v1
	v_bfe_u32 v8, v3, 16, 1
	v_add3_u32 v3, v3, v8, s90
	v_sub_f32_e32 v0, v77, v0
	ds_write_b16_d16_hi v2, v3 offset:384
	v_mul_f32_e32 v3, v0, v1
	s_waitcnt lgkmcnt(14)
; #define LAS __attribute__((address_space(3)))
; __device__ __forceinline__ bf16_t f2bf(float f) { unsigned u = __builtin_bit_cast(unsigned, f); return (bf16_t)((u + 0x7fffu + ((u >> 16) & 1u)) >> 16); }
; template <int DK, int DV, bool MLSTM>
; __device__ __forceinline__ void out_unit2(LAS unsigned char* lds, LAS unsigned char* ldstab, const OutArgs a, const int wv) {
;     ...
;         else { mean = t1 * (1.f / DV); inv = rsqrtf(fmaxf(t2 * (1.f / DV) - mean * mean, 0.f) + EPS); }
; #pragma unroll
;         for (int nb = 0; nb < NB; ++nb) { const int col = dh * (DV / 2) + 32 * nb + r32;
;             *(LAS bf16_t*)(lds + row * TP + col * 2) = f2bf((o[nb][r] - mean) * inv); }
;     }
;     __syncthreads();
;     constexpr int CPR = DV / 8;
; #pragma unroll 1
;     for (int id = tid; id < 128 * CPR; id += 512) { const int row = id / CPR, ch = id % CPR;
;         const u32x4 y = *(const LAS u32x4*)(lds + row * TP + ch * 16);
;         const f32x4 g0 = *(const f32x4*)(a.gain + 8 * ch), g1 = *(const f32x4*)(a.gain + 8 * ch + 4);
;         float yv[8] = {bf_lo(y.x), bf_hi(y.x), bf_lo(y.y), bf_hi(y.y), bf_lo(y.z), bf_hi(y.z), bf_lo(y.w), bf_hi(y.w)};
;         float gv[8];
;         if (MLSTM) { const u32x4 g = *(const u32x4*)(a.G + (size_t)row * a.ldg + 8 * ch);
;             gv[0] = bf_lo(g.x); gv[1] = bf_hi(g.x); gv[2] = bf_lo(g.y); gv[3] = bf_hi(g.y); gv[4] = bf_lo(g.z); gv[5] = bf_hi(g.z); gv[6] = bf_lo(g.w); gv[7] = bf_hi(g.w); }
;         else { const u32x2 g = *(const u32x2*)(a.G8 + (size_t)row * a.ldg8 + 8 * ch);
	v_pk_add_f32 v[0:1], v[128:129], v[4:5]
	s_nop 0
	v_pk_mul_f32 v[0:1], v[0:1], s[36:37] op_sel_hi:[1,0]
	s_nop 0
	v_fma_f32 v1, -v0, v0, v1
	v_max_f32_e32 v1, 0, v1
	v_add_f32_e32 v1, 0x358637bd, v1
	v_mul_f32_e32 v4, 0x4b800000, v1
	v_cmp_gt_f32_e32 vcc, s89, v1
	s_nop 1
	v_cndmask_b32_e32 v1, v1, v4, vcc
	v_rsq_f32_e32 v1, v1
	v_bfe_u32 v4, v3, 16, 1
	v_add3_u32 v3, v3, v4, s90
	ds_write_b16_d16_hi v2, v3 offset:448
	v_mul_f32_e32 v2, 0x45800000, v1
	v_cndmask_b32_e32 v1, v1, v2, vcc
	v_sub_f32_e32 v3, v30, v0
	v_mul_f32_e32 v3, v3, v1
	v_lshlrev_b32_e32 v2, 10, v162
	v_bfe_u32 v4, v3, 16, 1
	v_add3_u32 v3, v3, v4, s90
	v_add3_u32 v2, 0, v2, v16
	ds_write_b16_d16_hi v2, v3
	v_sub_f32_e32 v3, v14, v0
	v_mul_f32_e32 v3, v3, v1
	v_bfe_u32 v4, v3, 16, 1
	v_add3_u32 v3, v3, v4, s90
	ds_write_b16_d16_hi v2, v3 offset:64
	v_sub_f32_e32 v3, v46, v0
	v_mul_f32_e32 v3, v3, v1
	v_bfe_u32 v4, v3, 16, 1
	v_add3_u32 v3, v3, v4, s90
	ds_write_b16_d16_hi v2, v3 offset:128
	v_sub_f32_e32 v3, v62, v0
	v_mul_f32_e32 v3, v3, v1
	v_bfe_u32 v4, v3, 16, 1
	v_add3_u32 v3, v3, v4, s90
	ds_write_b16_d16_hi v2, v3 offset:192
	v_sub_f32_e32 v3, v110, v0
	v_mul_f32_e32 v3, v3, v1
	v_bfe_u32 v4, v3, 16, 1
	v_add3_u32 v3, v3, v4, s90
	ds_write_b16_d16_hi v2, v3 offset:256
	v_sub_f32_e32 v3, v126, v0
	v_mul_f32_e32 v3, v3, v1
	v_bfe_u32 v4, v3, 16, 1
	v_add3_u32 v3, v3, v4, s90
	ds_write_b16_d16_hi v2, v3 offset:320
	v_sub_f32_e32 v3, v94, v0
	v_mul_f32_e32 v3, v3, v1
	v_bfe_u32 v4, v3, 16, 1
	v_add3_u32 v3, v3, v4, s90
	v_sub_f32_e32 v0, v78, v0
	ds_write_b16_d16_hi v2, v3 offset:384
	v_mul_f32_e32 v3, v0, v1
	v_pk_add_f32 v[0:1], v[130:131], v[6:7]
	s_nop 0
	v_pk_mul_f32 v[0:1], v[0:1], s[36:37] op_sel_hi:[1,0]
	s_nop 0
	v_fma_f32 v1, -v0, v0, v1
	v_max_f32_e32 v1, 0, v1
	v_add_f32_e32 v1, 0x358637bd, v1
	v_mul_f32_e32 v4, 0x4b800000, v1
	v_cmp_gt_f32_e32 vcc, s89, v1
	s_nop 1
	v_cndmask_b32_e32 v1, v1, v4, vcc
	v_rsq_f32_e32 v1, v1
	v_bfe_u32 v4, v3, 16, 1
	v_add3_u32 v3, v3, v4, s90
	ds_write_b16_d16_hi v2, v3 offset:448
	v_mul_f32_e32 v2, 0x45800000, v1
	v_cndmask_b32_e32 v1, v1, v2, vcc
	v_sub_f32_e32 v3, v31, v0
	v_mul_f32_e32 v3, v3, v1
	v_lshlrev_b32_e32 v2, 10, v160
	v_bfe_u32 v4, v3, 16, 1
	v_add3_u32 v3, v3, v4, s90
	v_add3_u32 v2, 0, v2, v16
	ds_write_b16_d16_hi v2, v3
	v_sub_f32_e32 v3, v15, v0
	v_mul_f32_e32 v3, v3, v1
	v_bfe_u32 v4, v3, 16, 1
	v_add3_u32 v3, v3, v4, s90
	ds_write_b16_d16_hi v2, v3 offset:64
	v_sub_f32_e32 v3, v47, v0
	v_mul_f32_e32 v3, v3, v1
	v_bfe_u32 v4, v3, 16, 1
	v_add3_u32 v3, v3, v4, s90
	ds_write_b16_d16_hi v2, v3 offset:128
	v_sub_f32_e32 v3, v63, v0
	v_mul_f32_e32 v3, v3, v1
	v_bfe_u32 v4, v3, 16, 1
	v_add3_u32 v3, v3, v4, s90
	ds_write_b16_d16_hi v2, v3 offset:192
	v_sub_f32_e32 v3, v111, v0
	v_mul_f32_e32 v3, v3, v1
	v_bfe_u32 v4, v3, 16, 1
	v_add3_u32 v3, v3, v4, s90
	ds_write_b16_d16_hi v2, v3 offset:256
	v_sub_f32_e32 v3, v127, v0
	v_mul_f32_e32 v3, v3, v1
	v_bfe_u32 v4, v3, 16, 1
	v_add3_u32 v3, v3, v4, s90
	ds_write_b16_d16_hi v2, v3 offset:320
	v_sub_f32_e32 v3, v95, v0
	v_sub_f32_e32 v0, v79, v0
	v_mul_f32_e32 v3, v3, v1
	v_mul_f32_e32 v0, v0, v1
	v_bfe_u32 v4, v3, 16, 1
	v_bfe_u32 v1, v0, 16, 1
	v_add3_u32 v3, v3, v4, s90
	v_add3_u32 v0, v0, v1, s90
	v_cmp_gt_i32_e32 vcc, s88, v232
	ds_write_b16_d16_hi v2, v3 offset:384
	ds_write_b16_d16_hi v2, v0 offset:448
	s_lshl_b32 s4, s8, 2
	s_add_u32 s40, s24, s4
	s_addc_u32 s41, s25, 0
	s_lshl_b64 s[2:3], s[2:3], 11
	s_add_u32 s4, s53, s2
	s_addc_u32 s5, s54, s3
	s_add_u32 s42, s4, s8
	s_addc_u32 s43, s5, 0
	s_add_u32 s2, s55, s2
	s_addc_u32 s3, s56, s3
	s_add_u32 s44, s2, s8
	s_addc_u32 s45, s3, 0
	v_and_b32_e32 v6, 63, v232
	v_lshrrev_b32_e32 v7, 6, v232
	v_lshlrev_b32_e32 v8, 5, v6
	v_lshlrev_b32_e32 v5, 3, v6
	v_lshl_add_u32 v5, v7, 11, v5
	global_load_dwordx4 v[40:43], v8, s[40:41]
	global_load_dwordx4 v[44:47], v8, s[40:41] offset:16
	global_load_dwordx2 v[30:31], v5, s[42:43]
	v_add_u32_e32 v23, 0x4000, v5
	s_nop 0
	global_load_dwordx2 v[6:7], v23, s[42:43]
	v_add_u32_e32 v23, 0x4000, v23
	s_waitcnt lgkmcnt(0)
	s_barrier
	s_and_saveexec_b64 s[38:39], vcc
	s_cbranch_execz .LBB0_1826
	v_lshl_add_u32 v4, v232, 4, 0
	s_mov_b64 s[46:47], 0
	ds_read_b128 v[0:3], v4
	v_add_u32_e32 v4, 0x2000, v4
	v_mov_b32_e32 v162, v163
	s_mov_b32 s98, 0xbfb8aa3b
	s_mov_b32 s100, 0x41800000
	s_movk_i32 s46, 8
	s_waitcnt vmcnt(1)

; #define LAS __attribute__((address_space(3)))
; __device__ __forceinline__ bf16_t f2bf(float f) { unsigned u = __builtin_bit_cast(unsigned, f); return (bf16_t)((u + 0x7fffu + ((u >> 16) & 1u)) >> 16); }
; __device__ __forceinline__ int crow(int r, int hi) { return (r & 3) + 8 * (r >> 2) + 4 * hi; }
; __device__ __forceinline__ int crow(int r, int hi) { return (r & 3) + 8 * (r >> 2) + 4 * hi; }
; template <int DK, int DV, bool MLSTM>
; __device__ __forceinline__ void out_unit2(LAS unsigned char* lds, LAS unsigned char* ldstab, const OutArgs a, const int wv) {
;     ...
; #pragma unroll
;     for (int r = 0; r < 16; ++r) {
;         const int row = 32 * rb + crow(r, hi);
;         const float t1 = s1[r] + exch[((1 - dh) * 128 + row) * 2], t2 = s2[r] + exch[((1 - dh) * 128 + row) * 2 + 1];
;         float mean, inv;
;         if (MLSTM) { mean = 0.f; inv = rsqrtf(t2 * (1.f / DV) + EPS); }
;         else { mean = t1 * (1.f / DV); inv = rsqrtf(fmaxf(t2 * (1.f / DV) - mean * mean, 0.f) + EPS); }
; #pragma unroll
;         for (int nb = 0; nb < NB; ++nb) { const int col = dh * (DV / 2) + 32 * nb + r32;
;             *(LAS bf16_t*)(lds + row * TP + col * 2) = f2bf((o[nb][r] - mean) * inv); }
;     }
.LBB0_4313:
	s_or_b64 exec, exec, s[4:5]
	v_lshlrev_b32_e32 v164, 1, v219
	v_subrev_u32_e32 v164, s6, v164
	s_add_i32 s4, 0, 0x22100
	v_lshl_add_u32 v164, v164, 2, s4
	s_waitcnt vmcnt(0) lgkmcnt(0)
	s_barrier
	ds_read_b128 v[164:167], v164 offset:1024
	v_lshlrev_b32_e32 v168, 1, v217
	v_subrev_u32_e32 v168, s6, v168
	v_lshl_add_u32 v168, v168, 2, s4
	ds_read2_b64 v[168:171], v168 offset0:128 offset1:129
	s_waitcnt lgkmcnt(1)
	v_pk_add_f32 v[156:157], v[156:157], v[164:165]
	s_nop 0
	v_pk_mul_f32 v[156:157], v[156:157], s[26:27] op_sel_hi:[1,0]
	s_nop 0
	v_fma_f32 v157, -v156, v156, v157
	v_max_f32_e32 v157, 0, v157
	v_add_f32_e32 v157, 0x358637bd, v157
	v_mul_f32_e32 v164, 0x4b800000, v157
	v_cmp_gt_f32_e32 vcc, s89, v157
	v_sub_f32_e32 v16, v16, v156
	v_sub_f32_e32 v0, v0, v156
	v_cndmask_b32_e32 v157, v157, v164, vcc
	v_rsq_f32_e32 v157, v157
	v_or_b32_e32 v164, s6, v233
	v_mul_f32_e32 v165, 0x45800000, v157
	v_cndmask_b32_e32 v157, v157, v165, vcc
	v_mul_f32_e32 v16, v16, v157
	v_bfe_u32 v172, v16, 16, 1
	v_lshlrev_b32_e32 v165, 10, v219
	v_add3_u32 v172, v16, v172, s90
	v_lshlrev_b32_e32 v16, 1, v164
	v_mul_f32_e32 v0, v0, v157
	v_add3_u32 v164, 0, v165, v16
	v_bfe_u32 v165, v0, 16, 1
	v_add3_u32 v0, v0, v165, s90
	ds_write_b16_d16_hi v164, v0 offset:64
	v_sub_f32_e32 v0, v32, v156
	v_mul_f32_e32 v0, v0, v157
	v_bfe_u32 v32, v0, 16, 1
	v_add3_u32 v0, v0, v32, s90
	ds_write_b16_d16_hi v164, v0 offset:128
	v_sub_f32_e32 v0, v48, v156
	v_mul_f32_e32 v0, v0, v157
	v_bfe_u32 v32, v0, 16, 1
	v_add3_u32 v0, v0, v32, s90
	ds_write_b16_d16_hi v164, v0 offset:192
	v_sub_f32_e32 v0, v96, v156
	v_mul_f32_e32 v0, v0, v157
	v_bfe_u32 v32, v0, 16, 1
	v_add3_u32 v0, v0, v32, s90
	ds_write_b16_d16_hi v164, v0 offset:256
	v_sub_f32_e32 v0, v112, v156
	v_mul_f32_e32 v0, v0, v157
	v_bfe_u32 v32, v0, 16, 1
	v_add3_u32 v0, v0, v32, s90
	ds_write_b16_d16_hi v164, v0 offset:320
	v_sub_f32_e32 v0, v80, v156
	v_mul_f32_e32 v0, v0, v157
	v_bfe_u32 v32, v0, 16, 1
	v_add3_u32 v0, v0, v32, s90
	ds_write_b16_d16_hi v164, v0 offset:384
	v_sub_f32_e32 v0, v64, v156
	v_mul_f32_e32 v0, v0, v157
	v_pk_add_f32 v[156:157], v[158:159], v[166:167]
	ds_write_b16_d16_hi v164, v172
	v_pk_mul_f32 v[156:157], v[156:157], s[26:27] op_sel_hi:[1,0]
	s_nop 0
	v_fma_f32 v32, -v156, v156, v157
	v_max_f32_e32 v32, 0, v32
	v_add_f32_e32 v32, 0x358637bd, v32
	v_mul_f32_e32 v48, 0x4b800000, v32
	v_cmp_gt_f32_e32 vcc, s89, v32
	v_sub_f32_e32 v17, v17, v156
	v_sub_f32_e32 v1, v1, v156
	v_cndmask_b32_e32 v32, v32, v48, vcc
	v_rsq_f32_e32 v32, v32
	v_bfe_u32 v48, v0, 16, 1
	v_add3_u32 v0, v0, v48, s90
	ds_write_b16_d16_hi v164, v0 offset:448
	v_mul_f32_e32 v0, 0x45800000, v32
	v_cndmask_b32_e32 v0, v32, v0, vcc
	v_mul_f32_e32 v17, v17, v0
	v_lshlrev_b32_e32 v32, 10, v218
	v_bfe_u32 v48, v17, 16, 1
	v_add3_u32 v17, v17, v48, s90
	v_add3_u32 v32, 0, v32, v16
	v_mul_f32_e32 v1, v1, v0
	ds_write_b16_d16_hi v32, v17
	v_bfe_u32 v17, v1, 16, 1
	v_add3_u32 v1, v1, v17, s90
	ds_write_b16_d16_hi v32, v1 offset:64
	v_sub_f32_e32 v1, v33, v156
	v_mul_f32_e32 v1, v1, v0
	v_bfe_u32 v17, v1, 16, 1
	v_add3_u32 v1, v1, v17, s90
	ds_write_b16_d16_hi v32, v1 offset:128
	v_sub_f32_e32 v1, v49, v156
	v_mul_f32_e32 v1, v1, v0
	v_bfe_u32 v17, v1, 16, 1
	v_add3_u32 v1, v1, v17, s90
	ds_write_b16_d16_hi v32, v1 offset:192
	v_sub_f32_e32 v1, v97, v156
	v_mul_f32_e32 v1, v1, v0
	v_bfe_u32 v17, v1, 16, 1
	v_add3_u32 v1, v1, v17, s90
	ds_write_b16_d16_hi v32, v1 offset:256
	v_sub_f32_e32 v1, v113, v156
	v_mul_f32_e32 v1, v1, v0
	v_bfe_u32 v17, v1, 16, 1
	v_add3_u32 v1, v1, v17, s90
	ds_write_b16_d16_hi v32, v1 offset:320
	v_sub_f32_e32 v1, v81, v156
	v_mul_f32_e32 v1, v1, v0
	v_bfe_u32 v17, v1, 16, 1
	v_add3_u32 v1, v1, v17, s90
	ds_write_b16_d16_hi v32, v1 offset:384
	v_sub_f32_e32 v1, v65, v156
	v_mul_f32_e32 v17, v1, v0
	s_waitcnt lgkmcnt(14)
	v_pk_add_f32 v[0:1], v[152:153], v[168:169]
	s_nop 0
	v_pk_mul_f32 v[0:1], v[0:1], s[26:27] op_sel_hi:[1,0]
	s_nop 0
	v_fma_f32 v1, -v0, v0, v1
	v_max_f32_e32 v1, 0, v1
	v_add_f32_e32 v1, 0x358637bd, v1
	v_mul_f32_e32 v33, 0x4b800000, v1
	v_cmp_gt_f32_e32 vcc, s89, v1
	v_sub_f32_e32 v18, v18, v0
	v_sub_f32_e32 v2, v2, v0
	v_cndmask_b32_e32 v1, v1, v33, vcc
	v_rsq_f32_e32 v1, v1
	v_bfe_u32 v33, v17, 16, 1
	v_add3_u32 v17, v17, v33, s90
	ds_write_b16_d16_hi v32, v17 offset:448
	v_mul_f32_e32 v17, 0x45800000, v1
	v_cndmask_b32_e32 v1, v1, v17, vcc
	v_mul_f32_e32 v18, v18, v1
	v_lshlrev_b32_e32 v17, 10, v217
	v_bfe_u32 v32, v18, 16, 1
	v_add3_u32 v18, v18, v32, s90
	v_add3_u32 v17, 0, v17, v16
	v_mul_f32_e32 v2, v2, v1
	ds_write_b16_d16_hi v17, v18
	v_bfe_u32 v18, v2, 16, 1
	v_add3_u32 v2, v2, v18, s90
	ds_write_b16_d16_hi v17, v2 offset:64
	v_sub_f32_e32 v2, v34, v0
	v_mul_f32_e32 v2, v2, v1
	v_bfe_u32 v18, v2, 16, 1
	v_add3_u32 v2, v2, v18, s90
	ds_write_b16_d16_hi v17, v2 offset:128
	v_sub_f32_e32 v2, v50, v0
	v_mul_f32_e32 v2, v2, v1
	v_bfe_u32 v18, v2, 16, 1
	v_add3_u32 v2, v2, v18, s90
	ds_write_b16_d16_hi v17, v2 offset:192
	v_sub_f32_e32 v2, v98, v0
	v_mul_f32_e32 v2, v2, v1
	v_bfe_u32 v18, v2, 16, 1
	v_add3_u32 v2, v2, v18, s90
	ds_write_b16_d16_hi v17, v2 offset:256
	v_sub_f32_e32 v2, v114, v0
	v_mul_f32_e32 v2, v2, v1
	v_bfe_u32 v18, v2, 16, 1
	v_add3_u32 v2, v2, v18, s90
	ds_write_b16_d16_hi v17, v2 offset:320
	v_sub_f32_e32 v2, v82, v0
	v_mul_f32_e32 v2, v2, v1
	v_bfe_u32 v18, v2, 16, 1
	v_add3_u32 v2, v2, v18, s90
	v_sub_f32_e32 v0, v66, v0
	ds_write_b16_d16_hi v17, v2 offset:384
	v_mul_f32_e32 v2, v0, v1
	v_pk_add_f32 v[0:1], v[154:155], v[170:171]
	s_nop 0
	v_pk_mul_f32 v[0:1], v[0:1], s[26:27] op_sel_hi:[1,0]
	s_nop 0
	v_fma_f32 v1, -v0, v0, v1
	v_max_f32_e32 v1, 0, v1
; #define LAS __attribute__((address_space(3)))
; __device__ __forceinline__ bf16_t f2bf(float f) { unsigned u = __builtin_bit_cast(unsigned, f); return (bf16_t)((u + 0x7fffu + ((u >> 16) & 1u)) >> 16); }
; __device__ __forceinline__ int crow(int r, int hi) { return (r & 3) + 8 * (r >> 2) + 4 * hi; }
; __device__ __forceinline__ int crow(int r, int hi) { return (r & 3) + 8 * (r >> 2) + 4 * hi; }
; template <int DK, int DV, bool MLSTM>
; __device__ __forceinline__ void out_unit2(LAS unsigned char* lds, LAS unsigned char* ldstab, const OutArgs a, const int wv) {
;     ...
; #pragma unroll
;     for (int r = 0; r < 16; ++r) {
;         const int row = 32 * rb + crow(r, hi);
;         const float t1 = s1[r] + exch[((1 - dh) * 128 + row) * 2], t2 = s2[r] + exch[((1 - dh) * 128 + row) * 2 + 1];
;         float mean, inv;
;         if (MLSTM) { mean = 0.f; inv = rsqrtf(t2 * (1.f / DV) + EPS); }
;         else { mean = t1 * (1.f / DV); inv = rsqrtf(fmaxf(t2 * (1.f / DV) - mean * mean, 0.f) + EPS); }
; #pragma unroll
;         for (int nb = 0; nb < NB; ++nb) { const int col = dh * (DV / 2) + 32 * nb + r32;
;             *(LAS bf16_t*)(lds + row * TP + col * 2) = f2bf((o[nb][r] - mean) * inv); }
;     }
	v_add_f32_e32 v1, 0x358637bd, v1
	v_mul_f32_e32 v18, 0x4b800000, v1
	v_cmp_gt_f32_e32 vcc, s89, v1
	s_nop 1
	v_cndmask_b32_e32 v1, v1, v18, vcc
	v_rsq_f32_e32 v1, v1
	v_bfe_u32 v18, v2, 16, 1
	v_add3_u32 v2, v2, v18, s90
	ds_write_b16_d16_hi v17, v2 offset:448
	v_mul_f32_e32 v2, 0x45800000, v1
	v_cndmask_b32_e32 v1, v1, v2, vcc
	v_sub_f32_e32 v17, v19, v0
	v_mul_f32_e32 v17, v17, v1
	v_lshlrev_b32_e32 v2, 10, v216
	v_bfe_u32 v18, v17, 16, 1
	v_add3_u32 v17, v17, v18, s90
	v_add3_u32 v18, 0, v2, v16
	v_sub_f32_e32 v2, v3, v0
	v_mul_f32_e32 v2, v2, v1
	v_bfe_u32 v3, v2, 16, 1
	v_add3_u32 v2, v2, v3, s90
	ds_write_b16_d16_hi v18, v2 offset:64
	v_sub_f32_e32 v2, v35, v0
	v_mul_f32_e32 v2, v2, v1
	v_bfe_u32 v3, v2, 16, 1
	v_add3_u32 v2, v2, v3, s90
	ds_write_b16_d16_hi v18, v2 offset:128
	v_sub_f32_e32 v2, v51, v0
	v_mul_f32_e32 v2, v2, v1
	v_bfe_u32 v3, v2, 16, 1
	v_add3_u32 v2, v2, v3, s90
	ds_write_b16_d16_hi v18, v2 offset:192
	v_sub_f32_e32 v2, v99, v0
	v_mul_f32_e32 v2, v2, v1
	v_bfe_u32 v3, v2, 16, 1
	v_add3_u32 v2, v2, v3, s90
	ds_write_b16_d16_hi v18, v2 offset:256
	v_sub_f32_e32 v2, v115, v0
	v_mul_f32_e32 v2, v2, v1
	v_bfe_u32 v3, v2, 16, 1
	v_add3_u32 v2, v2, v3, s90
	ds_write_b16_d16_hi v18, v2 offset:320
	v_sub_f32_e32 v2, v83, v0
	v_sub_f32_e32 v0, v67, v0
	ds_write_b16_d16_hi v18, v17
	v_mul_f32_e32 v2, v2, v1
	v_mul_f32_e32 v17, v0, v1
	v_lshlrev_b32_e32 v0, 1, v215
	v_bfe_u32 v3, v2, 16, 1
	v_subrev_u32_e32 v0, s6, v0
	v_add3_u32 v2, v2, v3, s90
	v_lshl_add_u32 v0, v0, 2, s4
	ds_write_b16_d16_hi v18, v2 offset:384
	ds_read2_b64 v[0:3], v0 offset0:128 offset1:129
	v_lshlrev_b32_e32 v19, 1, v213
	v_subrev_u32_e32 v19, s6, v19
	v_lshl_add_u32 v19, v19, 2, s4
	ds_read2_b64 v[32:35], v19 offset0:128 offset1:129
	s_waitcnt lgkmcnt(1)
	v_pk_add_f32 v[0:1], v[148:149], v[0:1]
	s_nop 0
	v_pk_mul_f32 v[0:1], v[0:1], s[26:27] op_sel_hi:[1,0]
	s_nop 0
	v_fma_f32 v1, -v0, v0, v1
	v_max_f32_e32 v1, 0, v1
	v_add_f32_e32 v1, 0x358637bd, v1
	v_mul_f32_e32 v19, 0x4b800000, v1
	v_cmp_gt_f32_e32 vcc, s89, v1
	v_sub_f32_e32 v4, v4, v0
	s_nop 0
	v_cndmask_b32_e32 v1, v1, v19, vcc
	v_rsq_f32_e32 v1, v1
	v_bfe_u32 v19, v17, 16, 1
	v_add3_u32 v17, v17, v19, s90
	ds_write_b16_d16_hi v18, v17 offset:448
	v_mul_f32_e32 v17, 0x45800000, v1
	v_cndmask_b32_e32 v1, v1, v17, vcc
	v_sub_f32_e32 v18, v20, v0
	v_mul_f32_e32 v18, v18, v1
	v_lshlrev_b32_e32 v17, 10, v215
	v_bfe_u32 v19, v18, 16, 1
	v_add3_u32 v18, v18, v19, s90
	v_add3_u32 v17, 0, v17, v16
	v_mul_f32_e32 v4, v4, v1
	ds_write_b16_d16_hi v17, v18
	v_bfe_u32 v18, v4, 16, 1
	v_add3_u32 v4, v4, v18, s90
	ds_write_b16_d16_hi v17, v4 offset:64
	v_sub_f32_e32 v4, v36, v0
	v_mul_f32_e32 v4, v4, v1
	v_bfe_u32 v18, v4, 16, 1
	v_add3_u32 v4, v4, v18, s90
	ds_write_b16_d16_hi v17, v4 offset:128
	v_sub_f32_e32 v4, v52, v0
	v_mul_f32_e32 v4, v4, v1
	v_bfe_u32 v18, v4, 16, 1
	v_add3_u32 v4, v4, v18, s90
	ds_write_b16_d16_hi v17, v4 offset:192
	v_sub_f32_e32 v4, v100, v0
	v_mul_f32_e32 v4, v4, v1
	v_bfe_u32 v18, v4, 16, 1
	v_add3_u32 v4, v4, v18, s90
	ds_write_b16_d16_hi v17, v4 offset:256
	v_sub_f32_e32 v4, v116, v0
	v_mul_f32_e32 v4, v4, v1
	v_bfe_u32 v18, v4, 16, 1
	v_add3_u32 v4, v4, v18, s90
	ds_write_b16_d16_hi v17, v4 offset:320
	v_sub_f32_e32 v4, v84, v0
	v_mul_f32_e32 v4, v4, v1
	v_bfe_u32 v18, v4, 16, 1
	v_add3_u32 v4, v4, v18, s90
	v_sub_f32_e32 v0, v68, v0
	ds_write_b16_d16_hi v17, v4 offset:384
	v_mul_f32_e32 v4, v0, v1
	v_pk_add_f32 v[0:1], v[150:151], v[2:3]
	s_nop 0
	v_pk_mul_f32 v[0:1], v[0:1], s[26:27] op_sel_hi:[1,0]
	s_nop 0
	v_fma_f32 v1, -v0, v0, v1
	v_max_f32_e32 v1, 0, v1
	v_add_f32_e32 v1, 0x358637bd, v1
	v_mul_f32_e32 v2, 0x4b800000, v1
	v_cmp_gt_f32_e32 vcc, s89, v1
	v_sub_f32_e32 v3, v21, v0
	s_nop 0
	v_cndmask_b32_e32 v1, v1, v2, vcc
	v_rsq_f32_e32 v1, v1
	v_bfe_u32 v2, v4, 16, 1
	v_add3_u32 v2, v4, v2, s90
	ds_write_b16_d16_hi v17, v2 offset:448
	v_mul_f32_e32 v2, 0x45800000, v1
	v_cndmask_b32_e32 v1, v1, v2, vcc
	v_mul_f32_e32 v3, v3, v1
	v_lshlrev_b32_e32 v2, 10, v214
	v_bfe_u32 v4, v3, 16, 1
	v_add3_u32 v3, v3, v4, s90
	v_add3_u32 v2, 0, v2, v16
	ds_write_b16_d16_hi v2, v3
	v_sub_f32_e32 v3, v5, v0
	v_mul_f32_e32 v3, v3, v1
	v_bfe_u32 v4, v3, 16, 1
	v_add3_u32 v3, v3, v4, s90
	ds_write_b16_d16_hi v2, v3 offset:64
	v_sub_f32_e32 v3, v37, v0
	v_mul_f32_e32 v3, v3, v1
	v_bfe_u32 v4, v3, 16, 1
	v_add3_u32 v3, v3, v4, s90
	ds_write_b16_d16_hi v2, v3 offset:128
	v_sub_f32_e32 v3, v53, v0
	v_mul_f32_e32 v3, v3, v1
	v_bfe_u32 v4, v3, 16, 1
	v_add3_u32 v3, v3, v4, s90
	ds_write_b16_d16_hi v2, v3 offset:192
	v_sub_f32_e32 v3, v101, v0
	v_mul_f32_e32 v3, v3, v1
	v_bfe_u32 v4, v3, 16, 1
	v_add3_u32 v3, v3, v4, s90
	ds_write_b16_d16_hi v2, v3 offset:256
	v_sub_f32_e32 v3, v117, v0
	v_mul_f32_e32 v3, v3, v1
	v_bfe_u32 v4, v3, 16, 1
	v_add3_u32 v3, v3, v4, s90
	ds_write_b16_d16_hi v2, v3 offset:320
	v_sub_f32_e32 v3, v85, v0
	v_mul_f32_e32 v3, v3, v1
	v_bfe_u32 v4, v3, 16, 1
	v_add3_u32 v3, v3, v4, s90
	v_sub_f32_e32 v0, v69, v0
	ds_write_b16_d16_hi v2, v3 offset:384
	v_mul_f32_e32 v3, v0, v1
	s_waitcnt lgkmcnt(14)
; #define LAS __attribute__((address_space(3)))
; __device__ __forceinline__ bf16_t f2bf(float f) { unsigned u = __builtin_bit_cast(unsigned, f); return (bf16_t)((u + 0x7fffu + ((u >> 16) & 1u)) >> 16); }
; __device__ __forceinline__ int crow(int r, int hi) { return (r & 3) + 8 * (r >> 2) + 4 * hi; }
; __device__ __forceinline__ int crow(int r, int hi) { return (r & 3) + 8 * (r >> 2) + 4 * hi; }
; template <int DK, int DV, bool MLSTM>
; __device__ __forceinline__ void out_unit2(LAS unsigned char* lds, LAS unsigned char* ldstab, const OutArgs a, const int wv) {
;     ...
; #pragma unroll
;     for (int r = 0; r < 16; ++r) {
;         const int row = 32 * rb + crow(r, hi);
;         const float t1 = s1[r] + exch[((1 - dh) * 128 + row) * 2], t2 = s2[r] + exch[((1 - dh) * 128 + row) * 2 + 1];
;         float mean, inv;
;         if (MLSTM) { mean = 0.f; inv = rsqrtf(t2 * (1.f / DV) + EPS); }
;         else { mean = t1 * (1.f / DV); inv = rsqrtf(fmaxf(t2 * (1.f / DV) - mean * mean, 0.f) + EPS); }
; #pragma unroll
;         for (int nb = 0; nb < NB; ++nb) { const int col = dh * (DV / 2) + 32 * nb + r32;
;             *(LAS bf16_t*)(lds + row * TP + col * 2) = f2bf((o[nb][r] - mean) * inv); }
;     }
	v_pk_add_f32 v[0:1], v[144:145], v[32:33]
	s_nop 0
	v_pk_mul_f32 v[0:1], v[0:1], s[26:27] op_sel_hi:[1,0]
	s_nop 0
	v_fma_f32 v1, -v0, v0, v1
	v_max_f32_e32 v1, 0, v1
	v_add_f32_e32 v1, 0x358637bd, v1
	v_mul_f32_e32 v4, 0x4b800000, v1
	v_cmp_gt_f32_e32 vcc, s89, v1
	s_nop 1
	v_cndmask_b32_e32 v1, v1, v4, vcc
	v_rsq_f32_e32 v1, v1
	v_bfe_u32 v4, v3, 16, 1
	v_add3_u32 v3, v3, v4, s90
	ds_write_b16_d16_hi v2, v3 offset:448
	v_mul_f32_e32 v2, 0x45800000, v1
	v_cndmask_b32_e32 v1, v1, v2, vcc
	v_sub_f32_e32 v3, v22, v0
	v_mul_f32_e32 v3, v3, v1
	v_lshlrev_b32_e32 v2, 10, v213
	v_bfe_u32 v4, v3, 16, 1
	v_add3_u32 v3, v3, v4, s90
	v_add3_u32 v2, 0, v2, v16
	ds_write_b16_d16_hi v2, v3
	v_sub_f32_e32 v3, v6, v0
	v_mul_f32_e32 v3, v3, v1
	v_bfe_u32 v4, v3, 16, 1
	v_add3_u32 v3, v3, v4, s90
	ds_write_b16_d16_hi v2, v3 offset:64
	v_sub_f32_e32 v3, v38, v0
	v_mul_f32_e32 v3, v3, v1
	v_bfe_u32 v4, v3, 16, 1
	v_add3_u32 v3, v3, v4, s90
	ds_write_b16_d16_hi v2, v3 offset:128
	v_sub_f32_e32 v3, v54, v0
	v_mul_f32_e32 v3, v3, v1
	v_bfe_u32 v4, v3, 16, 1
	v_add3_u32 v3, v3, v4, s90
	ds_write_b16_d16_hi v2, v3 offset:192
	v_sub_f32_e32 v3, v102, v0
	v_mul_f32_e32 v3, v3, v1
	v_bfe_u32 v4, v3, 16, 1
	v_add3_u32 v3, v3, v4, s90
	ds_write_b16_d16_hi v2, v3 offset:256
	v_sub_f32_e32 v3, v118, v0
	v_mul_f32_e32 v3, v3, v1
	v_bfe_u32 v4, v3, 16, 1
	v_add3_u32 v3, v3, v4, s90
	ds_write_b16_d16_hi v2, v3 offset:320
	v_sub_f32_e32 v3, v86, v0
	v_mul_f32_e32 v3, v3, v1
	v_bfe_u32 v4, v3, 16, 1
	v_add3_u32 v3, v3, v4, s90
	v_sub_f32_e32 v0, v70, v0
	ds_write_b16_d16_hi v2, v3 offset:384
	v_mul_f32_e32 v3, v0, v1
	v_pk_add_f32 v[0:1], v[146:147], v[34:35]
	s_nop 0
	v_pk_mul_f32 v[0:1], v[0:1], s[26:27] op_sel_hi:[1,0]
	s_nop 0
	v_fma_f32 v1, -v0, v0, v1
	v_max_f32_e32 v1, 0, v1
	v_add_f32_e32 v1, 0x358637bd, v1
	v_mul_f32_e32 v4, 0x4b800000, v1
	v_cmp_gt_f32_e32 vcc, s89, v1
	s_nop 1
	v_cndmask_b32_e32 v1, v1, v4, vcc
	v_rsq_f32_e32 v1, v1
	v_bfe_u32 v4, v3, 16, 1
	v_add3_u32 v3, v3, v4, s90
	ds_write_b16_d16_hi v2, v3 offset:448
	v_mul_f32_e32 v2, 0x45800000, v1
	v_cndmask_b32_e32 v1, v1, v2, vcc
	v_sub_f32_e32 v3, v23, v0
	v_lshlrev_b32_e32 v2, 10, v212
	v_mul_f32_e32 v3, v3, v1
	v_bfe_u32 v4, v3, 16, 1
	v_add3_u32 v17, 0, v2, v16
	v_sub_f32_e32 v2, v7, v0
	v_add3_u32 v3, v3, v4, s90
	v_mul_f32_e32 v2, v2, v1
	ds_write_b16_d16_hi v17, v3
	v_bfe_u32 v3, v2, 16, 1
	v_add3_u32 v2, v2, v3, s90
	ds_write_b16_d16_hi v17, v2 offset:64
	v_sub_f32_e32 v2, v39, v0
	v_mul_f32_e32 v2, v2, v1
	v_bfe_u32 v3, v2, 16, 1
	v_add3_u32 v2, v2, v3, s90
	ds_write_b16_d16_hi v17, v2 offset:128
	v_sub_f32_e32 v2, v55, v0
	v_mul_f32_e32 v2, v2, v1
	v_bfe_u32 v3, v2, 16, 1
	v_add3_u32 v2, v2, v3, s90
	ds_write_b16_d16_hi v17, v2 offset:192
	v_sub_f32_e32 v2, v103, v0
	v_mul_f32_e32 v2, v2, v1
	v_bfe_u32 v3, v2, 16, 1
	v_add3_u32 v2, v2, v3, s90
	ds_write_b16_d16_hi v17, v2 offset:256
	v_sub_f32_e32 v2, v119, v0
	v_mul_f32_e32 v2, v2, v1
	v_bfe_u32 v3, v2, 16, 1
	v_add3_u32 v2, v2, v3, s90
	ds_write_b16_d16_hi v17, v2 offset:320
	v_sub_f32_e32 v2, v87, v0
	v_sub_f32_e32 v0, v71, v0
	v_mul_f32_e32 v2, v2, v1
	v_mul_f32_e32 v18, v0, v1
	v_lshlrev_b32_e32 v0, 1, v211
	v_bfe_u32 v3, v2, 16, 1
	v_subrev_u32_e32 v0, s6, v0
	v_add3_u32 v2, v2, v3, s90
	v_lshl_add_u32 v0, v0, 2, s4
	ds_write_b16_d16_hi v17, v2 offset:384
	ds_read2_b64 v[0:3], v0 offset0:128 offset1:129
	v_lshlrev_b32_e32 v4, 1, v209
	v_subrev_u32_e32 v4, s6, v4
	v_lshl_add_u32 v4, v4, 2, s4
	ds_read2_b64 v[4:7], v4 offset0:128 offset1:129
	s_waitcnt lgkmcnt(1)
	v_pk_add_f32 v[0:1], v[140:141], v[0:1]
	s_nop 0
	v_pk_mul_f32 v[0:1], v[0:1], s[26:27] op_sel_hi:[1,0]
	s_nop 0
	v_fma_f32 v1, -v0, v0, v1
	v_max_f32_e32 v1, 0, v1
	v_add_f32_e32 v1, 0x358637bd, v1
	v_mul_f32_e32 v19, 0x4b800000, v1
	v_cmp_gt_f32_e32 vcc, s89, v1
	v_sub_f32_e32 v8, v8, v0
	s_nop 0
	v_cndmask_b32_e32 v1, v1, v19, vcc
	v_rsq_f32_e32 v1, v1
	v_bfe_u32 v19, v18, 16, 1
	v_add3_u32 v18, v18, v19, s90
	ds_write_b16_d16_hi v17, v18 offset:448
	v_mul_f32_e32 v17, 0x45800000, v1
	v_cndmask_b32_e32 v1, v1, v17, vcc
	v_sub_f32_e32 v18, v24, v0
	v_mul_f32_e32 v18, v18, v1
	v_lshlrev_b32_e32 v17, 10, v211
	v_bfe_u32 v19, v18, 16, 1
	v_add3_u32 v18, v18, v19, s90
	v_add3_u32 v17, 0, v17, v16
	v_mul_f32_e32 v8, v8, v1
	ds_write_b16_d16_hi v17, v18
	v_bfe_u32 v18, v8, 16, 1
	v_add3_u32 v8, v8, v18, s90
	ds_write_b16_d16_hi v17, v8 offset:64
	v_sub_f32_e32 v8, v40, v0
	v_mul_f32_e32 v8, v8, v1
	v_bfe_u32 v18, v8, 16, 1
	v_add3_u32 v8, v8, v18, s90
	ds_write_b16_d16_hi v17, v8 offset:128
	v_sub_f32_e32 v8, v56, v0
	v_mul_f32_e32 v8, v8, v1
	v_bfe_u32 v18, v8, 16, 1
	v_add3_u32 v8, v8, v18, s90
	ds_write_b16_d16_hi v17, v8 offset:192
	v_sub_f32_e32 v8, v104, v0
	v_mul_f32_e32 v8, v8, v1
	v_bfe_u32 v18, v8, 16, 1
	v_add3_u32 v8, v8, v18, s90
	ds_write_b16_d16_hi v17, v8 offset:256
	v_sub_f32_e32 v8, v120, v0
	v_mul_f32_e32 v8, v8, v1
	v_bfe_u32 v18, v8, 16, 1
	v_add3_u32 v8, v8, v18, s90
	ds_write_b16_d16_hi v17, v8 offset:320
	v_sub_f32_e32 v8, v88, v0
	v_mul_f32_e32 v8, v8, v1
	v_bfe_u32 v18, v8, 16, 1
	v_add3_u32 v8, v8, v18, s90
	v_sub_f32_e32 v0, v72, v0
	ds_write_b16_d16_hi v17, v8 offset:384
	v_mul_f32_e32 v8, v0, v1
	v_pk_add_f32 v[0:1], v[142:143], v[2:3]
	s_nop 0
	v_pk_mul_f32 v[0:1], v[0:1], s[26:27] op_sel_hi:[1,0]
	s_nop 0
	v_fma_f32 v1, -v0, v0, v1
	v_max_f32_e32 v1, 0, v1
	v_add_f32_e32 v1, 0x358637bd, v1
	v_mul_f32_e32 v2, 0x4b800000, v1
	v_cmp_gt_f32_e32 vcc, s89, v1
	v_sub_f32_e32 v3, v25, v0
	s_nop 0
	v_cndmask_b32_e32 v1, v1, v2, vcc
	v_rsq_f32_e32 v1, v1
	v_bfe_u32 v2, v8, 16, 1
	v_add3_u32 v2, v8, v2, s90
	ds_write_b16_d16_hi v17, v2 offset:448
	v_mul_f32_e32 v2, 0x45800000, v1
	v_cndmask_b32_e32 v1, v1, v2, vcc
	v_mul_f32_e32 v3, v3, v1
	v_lshlrev_b32_e32 v2, 10, v210
	v_bfe_u32 v8, v3, 16, 1
	v_add3_u32 v3, v3, v8, s90
	v_add3_u32 v2, 0, v2, v16
	ds_write_b16_d16_hi v2, v3
	v_sub_f32_e32 v3, v9, v0
	v_mul_f32_e32 v3, v3, v1
	v_bfe_u32 v8, v3, 16, 1
	v_add3_u32 v3, v3, v8, s90
	ds_write_b16_d16_hi v2, v3 offset:64
	v_sub_f32_e32 v3, v41, v0
	v_mul_f32_e32 v3, v3, v1
	v_bfe_u32 v8, v3, 16, 1
	v_add3_u32 v3, v3, v8, s90
	ds_write_b16_d16_hi v2, v3 offset:128
	v_sub_f32_e32 v3, v57, v0
	v_mul_f32_e32 v3, v3, v1
	v_bfe_u32 v8, v3, 16, 1
	v_add3_u32 v3, v3, v8, s90
	ds_write_b16_d16_hi v2, v3 offset:192
	v_sub_f32_e32 v3, v105, v0
	v_mul_f32_e32 v3, v3, v1
	v_bfe_u32 v8, v3, 16, 1
	v_add3_u32 v3, v3, v8, s90
	ds_write_b16_d16_hi v2, v3 offset:256
	v_sub_f32_e32 v3, v121, v0
	v_mul_f32_e32 v3, v3, v1
	v_bfe_u32 v8, v3, 16, 1
	v_add3_u32 v3, v3, v8, s90
	ds_write_b16_d16_hi v2, v3 offset:320
	v_sub_f32_e32 v3, v89, v0
	v_mul_f32_e32 v3, v3, v1
	v_bfe_u32 v8, v3, 16, 1
	v_add3_u32 v3, v3, v8, s90
	v_sub_f32_e32 v0, v73, v0
	ds_write_b16_d16_hi v2, v3 offset:384
	v_mul_f32_e32 v3, v0, v1
	s_waitcnt lgkmcnt(14)
; #define LAS __attribute__((address_space(3)))
; __device__ __forceinline__ bf16_t f2bf(float f) { unsigned u = __builtin_bit_cast(unsigned, f); return (bf16_t)((u + 0x7fffu + ((u >> 16) & 1u)) >> 16); }
; __device__ __forceinline__ int crow(int r, int hi) { return (r & 3) + 8 * (r >> 2) + 4 * hi; }
; __device__ __forceinline__ int crow(int r, int hi) { return (r & 3) + 8 * (r >> 2) + 4 * hi; }
; template <int DK, int DV, bool MLSTM>
; __device__ __forceinline__ void out_unit2(LAS unsigned char* lds, LAS unsigned char* ldstab, const OutArgs a, const int wv) {
;     ...
; #pragma unroll
;     for (int r = 0; r < 16; ++r) {
;         const int row = 32 * rb + crow(r, hi);
;         const float t1 = s1[r] + exch[((1 - dh) * 128 + row) * 2], t2 = s2[r] + exch[((1 - dh) * 128 + row) * 2 + 1];
;         float mean, inv;
;         if (MLSTM) { mean = 0.f; inv = rsqrtf(t2 * (1.f / DV) + EPS); }
;         else { mean = t1 * (1.f / DV); inv = rsqrtf(fmaxf(t2 * (1.f / DV) - mean * mean, 0.f) + EPS); }
; #pragma unroll
;         for (int nb = 0; nb < NB; ++nb) { const int col = dh * (DV / 2) + 32 * nb + r32;
;             *(LAS bf16_t*)(lds + row * TP + col * 2) = f2bf((o[nb][r] - mean) * inv); }
;     }
	v_pk_add_f32 v[0:1], v[136:137], v[4:5]
	s_nop 0
	v_pk_mul_f32 v[0:1], v[0:1], s[26:27] op_sel_hi:[1,0]
	s_nop 0
	v_fma_f32 v1, -v0, v0, v1
	v_max_f32_e32 v1, 0, v1
	v_add_f32_e32 v1, 0x358637bd, v1
	v_mul_f32_e32 v4, 0x4b800000, v1
	v_cmp_gt_f32_e32 vcc, s89, v1
	s_nop 1
	v_cndmask_b32_e32 v1, v1, v4, vcc
	v_rsq_f32_e32 v1, v1
	v_bfe_u32 v4, v3, 16, 1
	v_add3_u32 v3, v3, v4, s90
	ds_write_b16_d16_hi v2, v3 offset:448
	v_mul_f32_e32 v2, 0x45800000, v1
	v_cndmask_b32_e32 v1, v1, v2, vcc
	v_sub_f32_e32 v3, v26, v0
	v_mul_f32_e32 v3, v3, v1
	v_lshlrev_b32_e32 v2, 10, v209
	v_bfe_u32 v4, v3, 16, 1
	v_add3_u32 v3, v3, v4, s90
	v_add3_u32 v2, 0, v2, v16
	ds_write_b16_d16_hi v2, v3
	v_sub_f32_e32 v3, v10, v0
	v_mul_f32_e32 v3, v3, v1
	v_bfe_u32 v4, v3, 16, 1
	v_add3_u32 v3, v3, v4, s90
	ds_write_b16_d16_hi v2, v3 offset:64
	v_sub_f32_e32 v3, v42, v0
	v_mul_f32_e32 v3, v3, v1
	v_bfe_u32 v4, v3, 16, 1
	v_add3_u32 v3, v3, v4, s90
	ds_write_b16_d16_hi v2, v3 offset:128
	v_sub_f32_e32 v3, v58, v0
	v_mul_f32_e32 v3, v3, v1
	v_bfe_u32 v4, v3, 16, 1
	v_add3_u32 v3, v3, v4, s90
	ds_write_b16_d16_hi v2, v3 offset:192
	v_sub_f32_e32 v3, v106, v0
	v_mul_f32_e32 v3, v3, v1
	v_bfe_u32 v4, v3, 16, 1
	v_add3_u32 v3, v3, v4, s90
	ds_write_b16_d16_hi v2, v3 offset:256
	v_sub_f32_e32 v3, v122, v0
	v_mul_f32_e32 v3, v3, v1
	v_bfe_u32 v4, v3, 16, 1
	v_add3_u32 v3, v3, v4, s90
	ds_write_b16_d16_hi v2, v3 offset:320
	v_sub_f32_e32 v3, v90, v0
	v_mul_f32_e32 v3, v3, v1
	v_bfe_u32 v4, v3, 16, 1
	v_add3_u32 v3, v3, v4, s90
	v_sub_f32_e32 v0, v74, v0
	ds_write_b16_d16_hi v2, v3 offset:384
	v_mul_f32_e32 v3, v0, v1
	v_pk_add_f32 v[0:1], v[138:139], v[6:7]
	s_nop 0
	v_pk_mul_f32 v[0:1], v[0:1], s[26:27] op_sel_hi:[1,0]
	s_nop 0
	v_fma_f32 v1, -v0, v0, v1
	v_max_f32_e32 v1, 0, v1
	v_add_f32_e32 v1, 0x358637bd, v1
	v_mul_f32_e32 v4, 0x4b800000, v1
	v_cmp_gt_f32_e32 vcc, s89, v1
	s_nop 1
	v_cndmask_b32_e32 v1, v1, v4, vcc
	v_rsq_f32_e32 v1, v1
	v_bfe_u32 v4, v3, 16, 1
	v_add3_u32 v3, v3, v4, s90
	ds_write_b16_d16_hi v2, v3 offset:448
	v_mul_f32_e32 v2, 0x45800000, v1
	v_cndmask_b32_e32 v1, v1, v2, vcc
	v_sub_f32_e32 v3, v27, v0
	v_lshlrev_b32_e32 v2, 10, v208
	v_mul_f32_e32 v3, v3, v1
	v_bfe_u32 v4, v3, 16, 1
	v_add3_u32 v8, 0, v2, v16
	v_sub_f32_e32 v2, v11, v0
	v_add3_u32 v3, v3, v4, s90
	v_mul_f32_e32 v2, v2, v1
	ds_write_b16_d16_hi v8, v3
	v_bfe_u32 v3, v2, 16, 1
	v_add3_u32 v2, v2, v3, s90
	ds_write_b16_d16_hi v8, v2 offset:64
	v_sub_f32_e32 v2, v43, v0
	v_mul_f32_e32 v2, v2, v1
	v_bfe_u32 v3, v2, 16, 1
	v_add3_u32 v2, v2, v3, s90
	ds_write_b16_d16_hi v8, v2 offset:128
	v_sub_f32_e32 v2, v59, v0
	v_mul_f32_e32 v2, v2, v1
	v_bfe_u32 v3, v2, 16, 1
	v_add3_u32 v2, v2, v3, s90
	ds_write_b16_d16_hi v8, v2 offset:192
	v_sub_f32_e32 v2, v107, v0
	v_mul_f32_e32 v2, v2, v1
	v_bfe_u32 v3, v2, 16, 1
	v_add3_u32 v2, v2, v3, s90
	ds_write_b16_d16_hi v8, v2 offset:256
	v_sub_f32_e32 v2, v123, v0
	v_mul_f32_e32 v2, v2, v1
	v_bfe_u32 v3, v2, 16, 1
	v_add3_u32 v2, v2, v3, s90
	ds_write_b16_d16_hi v8, v2 offset:320
	v_sub_f32_e32 v2, v91, v0
	v_sub_f32_e32 v0, v75, v0
	v_mul_f32_e32 v2, v2, v1
	v_mul_f32_e32 v9, v0, v1
	v_lshlrev_b32_e32 v0, 1, v207
	v_bfe_u32 v3, v2, 16, 1
	v_subrev_u32_e32 v0, s6, v0
	v_add3_u32 v2, v2, v3, s90
	v_lshl_add_u32 v0, v0, 2, s4
	ds_write_b16_d16_hi v8, v2 offset:384
	ds_read2_b64 v[0:3], v0 offset0:128 offset1:129
	v_lshlrev_b32_e32 v4, 1, v162
	v_subrev_u32_e32 v4, s6, v4
	v_lshl_add_u32 v4, v4, 2, s4
	ds_read2_b64 v[4:7], v4 offset0:128 offset1:129
	s_waitcnt lgkmcnt(1)
	v_pk_add_f32 v[0:1], v[132:133], v[0:1]
	s_nop 0
	v_pk_mul_f32 v[0:1], v[0:1], s[26:27] op_sel_hi:[1,0]
	s_nop 0
	v_fma_f32 v1, -v0, v0, v1
	v_max_f32_e32 v1, 0, v1
	v_add_f32_e32 v1, 0x358637bd, v1
	v_mul_f32_e32 v10, 0x4b800000, v1
	v_cmp_gt_f32_e32 vcc, s89, v1
	s_nop 1
	v_cndmask_b32_e32 v1, v1, v10, vcc
	v_rsq_f32_e32 v1, v1
	v_bfe_u32 v10, v9, 16, 1
	v_add3_u32 v9, v9, v10, s90
	ds_write_b16_d16_hi v8, v9 offset:448
	v_mul_f32_e32 v8, 0x45800000, v1
	v_cndmask_b32_e32 v1, v1, v8, vcc
	v_sub_f32_e32 v9, v28, v0
	v_mul_f32_e32 v9, v9, v1
	v_lshlrev_b32_e32 v8, 10, v207
	v_bfe_u32 v10, v9, 16, 1
	v_add3_u32 v9, v9, v10, s90
	v_add3_u32 v8, 0, v8, v16
	ds_write_b16_d16_hi v8, v9
	v_sub_f32_e32 v9, v12, v0
	v_mul_f32_e32 v9, v9, v1
	v_bfe_u32 v10, v9, 16, 1
	v_add3_u32 v9, v9, v10, s90
	ds_write_b16_d16_hi v8, v9 offset:64
	v_sub_f32_e32 v9, v44, v0
	v_mul_f32_e32 v9, v9, v1
	v_bfe_u32 v10, v9, 16, 1
	v_add3_u32 v9, v9, v10, s90
	ds_write_b16_d16_hi v8, v9 offset:128
	v_sub_f32_e32 v9, v60, v0
	v_mul_f32_e32 v9, v9, v1
	v_bfe_u32 v10, v9, 16, 1
	v_add3_u32 v9, v9, v10, s90
	ds_write_b16_d16_hi v8, v9 offset:192
	v_sub_f32_e32 v9, v108, v0
	v_mul_f32_e32 v9, v9, v1
	v_bfe_u32 v10, v9, 16, 1
	v_add3_u32 v9, v9, v10, s90
	ds_write_b16_d16_hi v8, v9 offset:256
	v_sub_f32_e32 v9, v124, v0
	v_mul_f32_e32 v9, v9, v1
	v_bfe_u32 v10, v9, 16, 1
	v_add3_u32 v9, v9, v10, s90
	ds_write_b16_d16_hi v8, v9 offset:320
	v_sub_f32_e32 v9, v92, v0
	v_mul_f32_e32 v9, v9, v1
	v_bfe_u32 v10, v9, 16, 1
	v_add3_u32 v9, v9, v10, s90
	v_sub_f32_e32 v0, v76, v0
	ds_write_b16_d16_hi v8, v9 offset:384
	v_mul_f32_e32 v9, v0, v1
	v_pk_add_f32 v[0:1], v[134:135], v[2:3]
	s_nop 0
	v_pk_mul_f32 v[0:1], v[0:1], s[26:27] op_sel_hi:[1,0]
	s_nop 0
	v_fma_f32 v1, -v0, v0, v1
	v_max_f32_e32 v1, 0, v1
	v_add_f32_e32 v1, 0x358637bd, v1
	v_mul_f32_e32 v2, 0x4b800000, v1
	v_cmp_gt_f32_e32 vcc, s89, v1
	v_sub_f32_e32 v3, v29, v0
	s_nop 0
	v_cndmask_b32_e32 v1, v1, v2, vcc
	v_rsq_f32_e32 v1, v1
	v_bfe_u32 v2, v9, 16, 1
	v_add3_u32 v2, v9, v2, s90
	ds_write_b16_d16_hi v8, v2 offset:448
	v_mul_f32_e32 v2, 0x45800000, v1
	v_cndmask_b32_e32 v1, v1, v2, vcc
	v_mul_f32_e32 v3, v3, v1
	v_lshlrev_b32_e32 v2, 10, v206
	v_bfe_u32 v8, v3, 16, 1
	v_add3_u32 v3, v3, v8, s90
	v_add3_u32 v2, 0, v2, v16
	ds_write_b16_d16_hi v2, v3
	v_sub_f32_e32 v3, v13, v0
	v_mul_f32_e32 v3, v3, v1
	v_bfe_u32 v8, v3, 16, 1
	v_add3_u32 v3, v3, v8, s90
	ds_write_b16_d16_hi v2, v3 offset:64
	v_sub_f32_e32 v3, v45, v0
	v_mul_f32_e32 v3, v3, v1
	v_bfe_u32 v8, v3, 16, 1
	v_add3_u32 v3, v3, v8, s90
	ds_write_b16_d16_hi v2, v3 offset:128
	v_sub_f32_e32 v3, v61, v0
	v_mul_f32_e32 v3, v3, v1
	v_bfe_u32 v8, v3, 16, 1
	v_add3_u32 v3, v3, v8, s90
	ds_write_b16_d16_hi v2, v3 offset:192
	v_sub_f32_e32 v3, v109, v0
	v_mul_f32_e32 v3, v3, v1
	v_bfe_u32 v8, v3, 16, 1
	v_add3_u32 v3, v3, v8, s90
	ds_write_b16_d16_hi v2, v3 offset:256
	v_sub_f32_e32 v3, v125, v0
	v_mul_f32_e32 v3, v3, v1
	v_bfe_u32 v8, v3, 16, 1
	v_add3_u32 v3, v3, v8, s90
	ds_write_b16_d16_hi v2, v3 offset:320
	v_sub_f32_e32 v3, v93, v0
	v_mul_f32_e32 v3, v3, v1
	v_bfe_u32 v8, v3, 16, 1
	v_add3_u32 v3, v3, v8, s90
	v_sub_f32_e32 v0, v77, v0
	ds_write_b16_d16_hi v2, v3 offset:384
	v_mul_f32_e32 v3, v0, v1
	s_waitcnt lgkmcnt(14)
; #define LAS __attribute__((address_space(3)))
; __device__ __forceinline__ bf16_t f2bf(float f) { unsigned u = __builtin_bit_cast(unsigned, f); return (bf16_t)((u + 0x7fffu + ((u >> 16) & 1u)) >> 16); }
; __device__ __forceinline__ int crow(int r, int hi) { return (r & 3) + 8 * (r >> 2) + 4 * hi; }
; __device__ __forceinline__ int crow(int r, int hi) { return (r & 3) + 8 * (r >> 2) + 4 * hi; }
; template <int DK, int DV, bool MLSTM>
; __device__ __forceinline__ void out_unit2(LAS unsigned char* lds, LAS unsigned char* ldstab, const OutArgs a, const int wv) {
;     ...
;     for (int r = 0; r < 16; ++r) {
;         const int row = 32 * rb + crow(r, hi);
;         const float t1 = s1[r] + exch[((1 - dh) * 128 + row) * 2], t2 = s2[r] + exch[((1 - dh) * 128 + row) * 2 + 1];
;         float mean, inv;
;         if (MLSTM) { mean = 0.f; inv = rsqrtf(t2 * (1.f / DV) + EPS); }
;         else { mean = t1 * (1.f / DV); inv = rsqrtf(fmaxf(t2 * (1.f / DV) - mean * mean, 0.f) + EPS); }
; #pragma unroll
;         for (int nb = 0; nb < NB; ++nb) { const int col = dh * (DV / 2) + 32 * nb + r32;
;             *(LAS bf16_t*)(lds + row * TP + col * 2) = f2bf((o[nb][r] - mean) * inv); }
;     }
;     __syncthreads();
;     constexpr int CPR = DV / 8;
; #pragma unroll 1
;     for (int id = tid; id < 128 * CPR; id += 512) { const int row = id / CPR, ch = id % CPR;
;         const u32x4 y = *(const LAS u32x4*)(lds + row * TP + ch * 16);
;         const f32x4 g0 = *(const f32x4*)(a.gain + 8 * ch), g1 = *(const f32x4*)(a.gain + 8 * ch + 4);
;         float yv[8] = {bf_lo(y.x), bf_hi(y.x), bf_lo(y.y), bf_hi(y.y), bf_lo(y.z), bf_hi(y.z), bf_lo(y.w), bf_hi(y.w)};
;         float gv[8];
;         if (MLSTM) { const u32x4 g = *(const u32x4*)(a.G + (size_t)row * a.ldg + 8 * ch);
;             gv[0] = bf_lo(g.x); gv[1] = bf_hi(g.x); gv[2] = bf_lo(g.y); gv[3] = bf_hi(g.y); gv[4] = bf_lo(g.z); gv[5] = bf_hi(g.z); gv[6] = bf_lo(g.w); gv[7] = bf_hi(g.w); }
;         else { const u32x2 g = *(const u32x2*)(a.G8 + (size_t)row * a.ldg8 + 8 * ch);
	v_pk_add_f32 v[0:1], v[128:129], v[4:5]
	s_nop 0
	v_pk_mul_f32 v[0:1], v[0:1], s[26:27] op_sel_hi:[1,0]
	s_nop 0
	v_fma_f32 v1, -v0, v0, v1
	v_max_f32_e32 v1, 0, v1
	v_add_f32_e32 v1, 0x358637bd, v1
	v_mul_f32_e32 v4, 0x4b800000, v1
	v_cmp_gt_f32_e32 vcc, s89, v1
	s_nop 1
	v_cndmask_b32_e32 v1, v1, v4, vcc
	v_rsq_f32_e32 v1, v1
	v_bfe_u32 v4, v3, 16, 1
	v_add3_u32 v3, v3, v4, s90
	ds_write_b16_d16_hi v2, v3 offset:448
	v_mul_f32_e32 v2, 0x45800000, v1
	v_cndmask_b32_e32 v1, v1, v2, vcc
	v_sub_f32_e32 v3, v30, v0
	v_mul_f32_e32 v3, v3, v1
	v_lshlrev_b32_e32 v2, 10, v162
	v_bfe_u32 v4, v3, 16, 1
	v_add3_u32 v3, v3, v4, s90
	v_add3_u32 v2, 0, v2, v16
	ds_write_b16_d16_hi v2, v3
	v_sub_f32_e32 v3, v14, v0
	v_mul_f32_e32 v3, v3, v1
	v_bfe_u32 v4, v3, 16, 1
	v_add3_u32 v3, v3, v4, s90
	ds_write_b16_d16_hi v2, v3 offset:64
	v_sub_f32_e32 v3, v46, v0
	v_mul_f32_e32 v3, v3, v1
	v_bfe_u32 v4, v3, 16, 1
	v_add3_u32 v3, v3, v4, s90
	ds_write_b16_d16_hi v2, v3 offset:128
	v_sub_f32_e32 v3, v62, v0
	v_mul_f32_e32 v3, v3, v1
	v_bfe_u32 v4, v3, 16, 1
	v_add3_u32 v3, v3, v4, s90
	ds_write_b16_d16_hi v2, v3 offset:192
	v_sub_f32_e32 v3, v110, v0
	v_mul_f32_e32 v3, v3, v1
	v_bfe_u32 v4, v3, 16, 1
	v_add3_u32 v3, v3, v4, s90
	ds_write_b16_d16_hi v2, v3 offset:256
	v_sub_f32_e32 v3, v126, v0
	v_mul_f32_e32 v3, v3, v1
	v_bfe_u32 v4, v3, 16, 1
	v_add3_u32 v3, v3, v4, s90
	ds_write_b16_d16_hi v2, v3 offset:320
	v_sub_f32_e32 v3, v94, v0
	v_mul_f32_e32 v3, v3, v1
	v_bfe_u32 v4, v3, 16, 1
	v_add3_u32 v3, v3, v4, s90
	v_sub_f32_e32 v0, v78, v0
	ds_write_b16_d16_hi v2, v3 offset:384
	v_mul_f32_e32 v3, v0, v1
	v_pk_add_f32 v[0:1], v[130:131], v[6:7]
	s_nop 0
	v_pk_mul_f32 v[0:1], v[0:1], s[26:27] op_sel_hi:[1,0]
	s_nop 0
	v_fma_f32 v1, -v0, v0, v1
	v_max_f32_e32 v1, 0, v1
	v_add_f32_e32 v1, 0x358637bd, v1
	v_mul_f32_e32 v4, 0x4b800000, v1
	v_cmp_gt_f32_e32 vcc, s89, v1
	s_nop 1
	v_cndmask_b32_e32 v1, v1, v4, vcc
	v_rsq_f32_e32 v1, v1
	v_bfe_u32 v4, v3, 16, 1
	v_add3_u32 v3, v3, v4, s90
	ds_write_b16_d16_hi v2, v3 offset:448
	v_mul_f32_e32 v2, 0x45800000, v1
	v_cndmask_b32_e32 v1, v1, v2, vcc
	v_sub_f32_e32 v3, v31, v0
	v_mul_f32_e32 v3, v3, v1
	v_lshlrev_b32_e32 v2, 10, v160
	v_bfe_u32 v4, v3, 16, 1
	v_add3_u32 v3, v3, v4, s90
	v_add3_u32 v2, 0, v2, v16
	ds_write_b16_d16_hi v2, v3
	v_sub_f32_e32 v3, v15, v0
	v_mul_f32_e32 v3, v3, v1
	v_bfe_u32 v4, v3, 16, 1
	v_add3_u32 v3, v3, v4, s90
	ds_write_b16_d16_hi v2, v3 offset:64
	v_sub_f32_e32 v3, v47, v0
	v_mul_f32_e32 v3, v3, v1
	v_bfe_u32 v4, v3, 16, 1
	v_add3_u32 v3, v3, v4, s90
	ds_write_b16_d16_hi v2, v3 offset:128
	v_sub_f32_e32 v3, v63, v0
	v_mul_f32_e32 v3, v3, v1
	v_bfe_u32 v4, v3, 16, 1
	v_add3_u32 v3, v3, v4, s90
	ds_write_b16_d16_hi v2, v3 offset:192
	v_sub_f32_e32 v3, v111, v0
	v_mul_f32_e32 v3, v3, v1
	v_bfe_u32 v4, v3, 16, 1
	v_add3_u32 v3, v3, v4, s90
	ds_write_b16_d16_hi v2, v3 offset:256
	v_sub_f32_e32 v3, v127, v0
	v_mul_f32_e32 v3, v3, v1
	v_bfe_u32 v4, v3, 16, 1
	v_add3_u32 v3, v3, v4, s90
	ds_write_b16_d16_hi v2, v3 offset:320
	v_sub_f32_e32 v3, v95, v0
	v_sub_f32_e32 v0, v79, v0
	v_mul_f32_e32 v3, v3, v1
	v_mul_f32_e32 v0, v0, v1
	v_bfe_u32 v4, v3, 16, 1
	v_bfe_u32 v1, v0, 16, 1
	v_add3_u32 v3, v3, v4, s90
	v_add3_u32 v0, v0, v1, s90
	v_cmp_gt_i32_e32 vcc, s88, v232
	ds_write_b16_d16_hi v2, v3 offset:384
	ds_write_b16_d16_hi v2, v0 offset:448
	s_lshl_b32 s4, s8, 2
	s_add_u32 s38, s51, s4
	s_addc_u32 s39, s52, 0
	s_lshl_b64 s[2:3], s[2:3], 11
	s_add_u32 s4, s53, s2
	s_addc_u32 s5, s54, s3
	s_add_u32 s40, s4, s8
	s_addc_u32 s41, s5, 0
	s_add_u32 s2, s55, s2
	s_addc_u32 s3, s56, s3
	s_add_u32 s42, s2, s8
	s_addc_u32 s43, s3, 0
	v_and_b32_e32 v6, 63, v232
	v_lshrrev_b32_e32 v7, 6, v232
	v_lshlrev_b32_e32 v8, 5, v6
	v_lshlrev_b32_e32 v5, 3, v6
	v_lshl_add_u32 v5, v7, 11, v5
	global_load_dwordx4 v[40:43], v8, s[38:39]
	global_load_dwordx4 v[44:47], v8, s[38:39] offset:16
	global_load_dwordx2 v[30:31], v5, s[40:41]
	v_add_u32_e32 v23, 0x4000, v5
	s_nop 0
	global_load_dwordx2 v[6:7], v23, s[40:41]
	v_add_u32_e32 v23, 0x4000, v23
	s_waitcnt lgkmcnt(0)
	s_barrier
	s_and_saveexec_b64 s[36:37], vcc
	s_cbranch_execz .LBB0_4301
	v_lshl_add_u32 v4, v232, 4, 0
	s_mov_b64 s[44:45], 0
	ds_read_b128 v[0:3], v4
	v_add_u32_e32 v4, 0x2000, v4
	v_mov_b32_e32 v162, v163
	s_mov_b32 s98, 0xbfb8aa3b
	s_mov_b32 s100, 0x41800000
	s_movk_i32 s44, 8
	s_waitcnt vmcnt(1)
